# pre-conversion slots spread over all column windows; per-queue rotation of the column-tile order in both MoE queues (queues stream different column windows of the weight rows); 3 K-tiles in flight in
# speedup vs baseline: 1.0408x; 1.0094x over previous
; #define LAS3 __attribute__((address_space(3)))
; #define G_SCHED __builtin_amdgcn_sched_barrier(0)
; __device__ __forceinline__ int lane_id() { int r; asm volatile("v_mbcnt_lo_u32_b32 %0, -1, 0\n\tv_mbcnt_hi_u32_b32 %0, -1, %0" : "=v"(r)); return r; }
; #define CI_LOAD(R, kt) do { _Pragma("unroll") for (int _j = 0; _j < 16; ++_j) R[_j] = __builtin_nontemporal_load((const f32x4*)(src + (size_t)((kt) * 128 + _j) * LDB)); } while (0)
; template <int LDB>
; __device__ __forceinline__ void convert_image(const float* __restrict__ W, int col0, int col1, unsigned char* __restrict__ img, LAS3 char* lds, int wid) {
;     int lane = lane_id(); asm volatile("" : "+v"(lane));
;     const int n4 = lane, half = n4 >> 5, nloc = (n4 & 31) * 4;
;     const float* src = W + (size_t)(wid * 16) * LDB + ((n4 < 32) ? col0 + n4 * 4 : col1 + (n4 - 32) * 4);
;     const unsigned cpo = (unsigned)(wid * 4096 + lane * 16);
;     ...
;     f32x4 ra[16], rb[16];
;     CI_LOAD(ra, 0);
;     for (int kt = 0; kt < 16; kt += 2) {
;         CI_LOAD(rb, kt + 1); G_SCHED;
; __global__ void __launch_bounds__(512, 2) k_mega(Params p) {
;     ...
;     { GemmArgs g{}; g.A = p.xn; g.C = p.proj; g.R = (const float*)p.proj2;
;       for (int u = vb; u < 32 * 16 + 256; u += nb) {
;           int pm, pn, kh = -1;
;           if (nb == 256) { const int r = u >> 8, x = (u >> 5) & 7, j = u & 31; pm = 8 * (x & 3) + (j & 7);
;               if (u < 32 * 16) pn = 8 * r + 4 * (x >> 2) + (j >> 3); else { pn = 16 + (j >> 3); kh = x >> 2; } }
;           else if (u < 32 * 16) { pm = u & 31; pn = u >> 5; }
;           else { const int v = u - 32 * 16; pn = 16 + (v >> 6); pm = v & 31; kh = (v >> 5) & 1; }
;           gemm_tile_img<0>(g, pm, pn, 0, 0, T, lds, wid, p.img_in + (size_t)pn * 1048576, TileSync{}, kh); } }
.LBB0_74:
	s_add_i32 s87, s87, s80
	s_cmpk_gt_i32 s87, 0x3ff
	s_cbranch_scc1 .LBB0_116
.LBB0_75:
	s_cmpk_lg_i32 s80, 0x100
	s_cbranch_scc1 .Lpc_skip
	s_lshr_b32 s1, s35, 3
	s_lshr_b32 s4, s35, 5
	s_add_u32 s1, s1, s4
	s_and_b32 s1, s1, 3
	s_lshr_b32 s0, s87, 8
	s_cmp_lg_u32 s0, s1
	s_cbranch_scc1 .Lpc_skip
	v_readlane_b32 s0, v254, 18
	v_readlane_b32 s1, v254, 19
	s_lshr_b32 s100, s35, 5
	s_and_b32 s101, s35, 31
	s_sub_u32 s88, s101, 16
	s_lshr_b32 s4, s88, 3
	s_lshl_b32 s4, s4, 3
	s_add_u32 s4, s4, s100
	s_and_b32 s5, s88, 7
	s_cmp_lt_u32 s101, 16
	s_cselect_b32 vcc_lo, 1, 0
	s_cselect_b32 s4, s100, s4
	s_cselect_b32 s5, s101, s5
	s_sub_u32 s0, s0, 0x140
	s_subb_u32 s1, s1, 0
	s_lshl_b32 s6, vcc_lo, 4
	s_sub_u32 s6, 0x80, s6
	s_lshl_b32 s88, vcc_lo, 3
	s_sub_u32 s88, 0x120, s88
	s_load_dwordx2 s[100:101], s[0:1], s6
	s_load_dwordx2 s[6:7], s[0:1], s88
	s_load_dwordx2 s[0:1], s[0:1], 0x128
	s_waitcnt lgkmcnt(0)
	s_add_u32 s88, vcc_lo, 24
	s_lshl_b32 s88, s4, s88
	s_add_u32 s100, s100, s88
	s_addc_u32 s101, s101, 0
	s_sub_u32 s88, 10, vcc_lo
	s_lshl_b32 s88, s5, s88
	s_add_u32 s100, s100, s88
	s_addc_u32 s101, s101, 0
	s_lshr_b32 vcc_hi, s75, 6
	s_add_u32 s88, vcc_lo, 17
	s_lshl_b32 s88, vcc_hi, s88
	s_add_u32 s100, s100, s88
	s_addc_u32 s101, s101, 0
	s_add_u32 s88, vcc_lo, 3
	s_lshl_b32 s88, s4, s88
	s_add_u32 s88, s88, s5
	s_lshl_b32 s4, s88, 19
	s_add_u32 s6, s6, s4
	s_addc_u32 s7, s7, 0
	s_xor_b32 s4, vcc_lo, 1
	s_lshl_b32 s4, s4, 9
	s_add_u32 s4, s4, s88
	s_lshl_b32 s4, s4, 2
	s_add_u32 s0, s0, s4
	s_addc_u32 s1, s1, 0
	v_mbcnt_lo_u32_b32 v131, -1, 0
	v_mbcnt_hi_u32_b32 v131, -1, v131
	s_add_u32 s4, vcc_lo, 13
	s_lshl_b32 s5, 1, s4
	s_lshl_b32 s88, vcc_lo, 2
	s_add_u32 s88, s88, 9
	s_lshl_b32 s88, 1, s88
	v_and_b32_e32 v132, 31, v131
	v_lshrrev_b32_e32 v150, 5, v131
	v_lshlrev_b32_e32 v132, 4, v132
	v_mad_u32_u24 v132, v150, s88, v132
	v_add_u32_e32 v133, s5, v132
	v_add_u32_e32 v134, s5, v133
	v_add_u32_e32 v135, s5, v134
	v_add_u32_e32 v136, s5, v135
	v_add_u32_e32 v137, s5, v136
	v_add_u32_e32 v138, s5, v137
	v_add_u32_e32 v139, s5, v138
	v_add_u32_e32 v140, s5, v139
	v_add_u32_e32 v141, s5, v140
	v_add_u32_e32 v142, s5, v141
	v_add_u32_e32 v143, s5, v142
	v_add_u32_e32 v144, s5, v143
	v_add_u32_e32 v145, s5, v144
	v_add_u32_e32 v146, s5, v145
	v_add_u32_e32 v147, s5, v146
	v_and_b32_e32 v151, 3, v131
	v_lshlrev_b32_e32 v151, 1, v151
	v_xor_b32_e32 v148, vcc_hi, v151
	v_or_b32_e32 v151, 1, v151
	v_xor_b32_e32 v149, vcc_hi, v151
	v_lshlrev_b32_e32 v148, 4, v148
	v_lshlrev_b32_e32 v149, 4, v149
	v_and_b32_e32 v151, 31, v131
	v_lshlrev_b32_e32 v151, 9, v151
	v_lshl_add_u32 v151, v150, 14, v151
	v_add_u32_e32 v148, v148, v151
	v_add_u32_e32 v149, v149, v151
	v_add_u32_e32 v149, 0x100, v149
	v_lshlrev_b32_e32 v150, 4, v131
	s_lshl_b32 s4, vcc_hi, 12
	v_add_u32_e32 v150, s4, v150
	s_lshl_b32 s88, s5, 7
	s_mov_b32 s5, 0x3b800000
	global_load_dwordx4 v[0:3], v132, s[100:101] nt
	global_load_dwordx4 v[4:7], v133, s[100:101] nt
	global_load_dwordx4 v[8:11], v134, s[100:101] nt
	global_load_dwordx4 v[12:15], v135, s[100:101] nt
	global_load_dwordx4 v[16:19], v136, s[100:101] nt
	global_load_dwordx4 v[20:23], v137, s[100:101] nt
	global_load_dwordx4 v[24:27], v138, s[100:101] nt
	global_load_dwordx4 v[28:31], v139, s[100:101] nt
	global_load_dwordx4 v[32:35], v140, s[100:101] nt
	global_load_dwordx4 v[36:39], v141, s[100:101] nt
	global_load_dwordx4 v[40:43], v142, s[100:101] nt
	global_load_dwordx4 v[44:47], v143, s[100:101] nt
	global_load_dwordx4 v[48:51], v144, s[100:101] nt
	global_load_dwordx4 v[52:55], v145, s[100:101] nt
	global_load_dwordx4 v[56:59], v146, s[100:101] nt
	global_load_dwordx4 v[60:63], v147, s[100:101] nt
	s_add_u32 s100, s100, s88
	s_addc_u32 s101, s101, 0
	global_load_dwordx4 v[64:67], v132, s[100:101] nt
	global_load_dwordx4 v[68:71], v133, s[100:101] nt
	global_load_dwordx4 v[72:75], v134, s[100:101] nt
	global_load_dwordx4 v[76:79], v135, s[100:101] nt
	global_load_dwordx4 v[80:83], v136, s[100:101] nt
	global_load_dwordx4 v[84:87], v137, s[100:101] nt
	global_load_dwordx4 v[88:91], v138, s[100:101] nt
	global_load_dwordx4 v[92:95], v139, s[100:101] nt
	global_load_dwordx4 v[96:99], v140, s[100:101] nt
	global_load_dwordx4 v[100:103], v141, s[100:101] nt
	global_load_dwordx4 v[104:107], v142, s[100:101] nt
	global_load_dwordx4 v[108:111], v143, s[100:101] nt
	global_load_dwordx4 v[112:115], v144, s[100:101] nt
	global_load_dwordx4 v[116:119], v145, s[100:101] nt
	global_load_dwordx4 v[120:123], v146, s[100:101] nt
	global_load_dwordx4 v[124:127], v147, s[100:101] nt
	s_add_u32 s100, s100, s88
	s_addc_u32 s101, s101, 0
	global_load_dwordx4 v[184:187], v132, s[100:101] nt
	global_load_dwordx4 v[188:191], v133, s[100:101] nt
	global_load_dwordx4 v[192:195], v134, s[100:101] nt
	global_load_dwordx4 v[196:199], v135, s[100:101] nt
	global_load_dwordx4 v[200:203], v136, s[100:101] nt
	global_load_dwordx4 v[204:207], v137, s[100:101] nt
	global_load_dwordx4 v[208:211], v138, s[100:101] nt
	global_load_dwordx4 v[212:215], v139, s[100:101] nt
	global_load_dwordx4 v[216:219], v140, s[100:101] nt
	global_load_dwordx4 v[220:223], v141, s[100:101] nt
	global_load_dwordx4 v[224:227], v142, s[100:101] nt
	global_load_dwordx4 v[228:231], v143, s[100:101] nt
	global_load_dwordx4 v[232:235], v144, s[100:101] nt
	global_load_dwordx4 v[236:239], v145, s[100:101] nt
	global_load_dwordx4 v[240:243], v146, s[100:101] nt
	global_load_dwordx4 v[244:247], v147, s[100:101] nt
	s_waitcnt vmcnt(32)
; #define G_SCHED __builtin_amdgcn_sched_barrier(0)
; #define CI_LOAD(R, kt) do { _Pragma("unroll") for (int _j = 0; _j < 16; ++_j) R[_j] = __builtin_nontemporal_load((const f32x4*)(src + (size_t)((kt) * 128 + _j) * LDB)); } while (0)
; template <int LDB>
; __device__ __forceinline__ void convert_image(const float* __restrict__ W, int col0, int col1, unsigned char* __restrict__ img, LAS3 char* lds, int wid) {
;     ...
;     f32x4 ra[16], rb[16];
;     CI_LOAD(ra, 0);
;     for (int kt = 0; kt < 16; kt += 2) {
;         CI_LOAD(rb, kt + 1); G_SCHED;
;         CI_CONV(ra, kt); G_SCHED;
;         CI_LOAD(ra, (kt + 2 < 16) ? kt + 2 : 15); G_SCHED;
;         CI_CONV(rb, kt + 1); G_SCHED;
;     }
	v_cvt_scalef32_pk_fp8_f32 v152, v0, v4, s5
	v_cvt_scalef32_pk_fp8_f32 v156, v1, v5, s5
	v_cvt_scalef32_pk_fp8_f32 v160, v2, v6, s5
	v_cvt_scalef32_pk_fp8_f32 v164, v3, v7, s5
	v_cvt_scalef32_pk_fp8_f32 v153, v16, v20, s5
	v_cvt_scalef32_pk_fp8_f32 v157, v17, v21, s5
	v_cvt_scalef32_pk_fp8_f32 v161, v18, v22, s5
	v_cvt_scalef32_pk_fp8_f32 v165, v19, v23, s5
	v_cvt_scalef32_pk_fp8_f32 v154, v32, v36, s5
	v_cvt_scalef32_pk_fp8_f32 v158, v33, v37, s5
	v_cvt_scalef32_pk_fp8_f32 v162, v34, v38, s5
	v_cvt_scalef32_pk_fp8_f32 v166, v35, v39, s5
	v_cvt_scalef32_pk_fp8_f32 v155, v48, v52, s5
	v_cvt_scalef32_pk_fp8_f32 v159, v49, v53, s5
	v_cvt_scalef32_pk_fp8_f32 v163, v50, v54, s5
	v_cvt_scalef32_pk_fp8_f32 v167, v51, v55, s5
	v_cvt_scalef32_pk_fp8_f32 v152, v8, v12, s5 op_sel:[0,0,0,1]
	v_cvt_scalef32_pk_fp8_f32 v156, v9, v13, s5 op_sel:[0,0,0,1]
	v_cvt_scalef32_pk_fp8_f32 v160, v10, v14, s5 op_sel:[0,0,0,1]
	v_cvt_scalef32_pk_fp8_f32 v164, v11, v15, s5 op_sel:[0,0,0,1]
	v_cvt_scalef32_pk_fp8_f32 v153, v24, v28, s5 op_sel:[0,0,0,1]
	v_cvt_scalef32_pk_fp8_f32 v157, v25, v29, s5 op_sel:[0,0,0,1]
	v_cvt_scalef32_pk_fp8_f32 v161, v26, v30, s5 op_sel:[0,0,0,1]
	v_cvt_scalef32_pk_fp8_f32 v165, v27, v31, s5 op_sel:[0,0,0,1]
	v_cvt_scalef32_pk_fp8_f32 v154, v40, v44, s5 op_sel:[0,0,0,1]
	v_cvt_scalef32_pk_fp8_f32 v158, v41, v45, s5 op_sel:[0,0,0,1]
	v_cvt_scalef32_pk_fp8_f32 v162, v42, v46, s5 op_sel:[0,0,0,1]
	v_cvt_scalef32_pk_fp8_f32 v166, v43, v47, s5 op_sel:[0,0,0,1]
	v_cvt_scalef32_pk_fp8_f32 v155, v56, v60, s5 op_sel:[0,0,0,1]
	v_cvt_scalef32_pk_fp8_f32 v159, v57, v61, s5 op_sel:[0,0,0,1]
	v_cvt_scalef32_pk_fp8_f32 v163, v58, v62, s5 op_sel:[0,0,0,1]
	v_cvt_scalef32_pk_fp8_f32 v167, v59, v63, s5 op_sel:[0,0,0,1]
	s_add_u32 s100, s100, s88
	s_addc_u32 s101, s101, 0
	global_load_dwordx4 v[0:3], v132, s[100:101] nt
	global_load_dwordx4 v[4:7], v133, s[100:101] nt
	global_load_dwordx4 v[8:11], v134, s[100:101] nt
	global_load_dwordx4 v[12:15], v135, s[100:101] nt
	global_load_dwordx4 v[16:19], v136, s[100:101] nt
	global_load_dwordx4 v[20:23], v137, s[100:101] nt
	global_load_dwordx4 v[24:27], v138, s[100:101] nt
	global_load_dwordx4 v[28:31], v139, s[100:101] nt
	global_load_dwordx4 v[32:35], v140, s[100:101] nt
	global_load_dwordx4 v[36:39], v141, s[100:101] nt
	global_load_dwordx4 v[40:43], v142, s[100:101] nt
	global_load_dwordx4 v[44:47], v143, s[100:101] nt
	global_load_dwordx4 v[48:51], v144, s[100:101] nt
	global_load_dwordx4 v[52:55], v145, s[100:101] nt
	global_load_dwordx4 v[56:59], v146, s[100:101] nt
	global_load_dwordx4 v[60:63], v147, s[100:101] nt
	ds_write_b128 v148, v[152:155] offset:0
	ds_write_b128 v148, v[156:159] offset:128
	ds_write_b128 v149, v[160:163] offset:0
	ds_write_b128 v149, v[164:167] offset:128
	s_waitcnt lgkmcnt(0)
	s_barrier
	ds_read_b128 v[168:171], v150 offset:0
	ds_read_b128 v[172:175], v150 offset:1024
	ds_read_b128 v[176:179], v150 offset:2048
	ds_read_b128 v[180:183], v150 offset:3072
	s_waitcnt lgkmcnt(3)
	global_store_dwordx4 v150, v[168:171], s[6:7] sc1
	s_waitcnt lgkmcnt(2)
	global_store_dwordx4 v150, v[172:175], s[6:7] offset:1024 sc1
	s_waitcnt lgkmcnt(1)
	global_store_dwordx4 v150, v[176:179], s[6:7] offset:2048 sc1
	s_waitcnt lgkmcnt(0)
	global_store_dwordx4 v150, v[180:183], s[6:7] offset:3072 sc1
	s_add_u32 s6, s6, 0x8000
	s_addc_u32 s7, s7, 0
	s_waitcnt vmcnt(36)
	v_cvt_scalef32_pk_fp8_f32 v152, v64, v68, s5
	v_cvt_scalef32_pk_fp8_f32 v156, v65, v69, s5
	v_cvt_scalef32_pk_fp8_f32 v160, v66, v70, s5
	v_cvt_scalef32_pk_fp8_f32 v164, v67, v71, s5
	v_cvt_scalef32_pk_fp8_f32 v153, v80, v84, s5
	v_cvt_scalef32_pk_fp8_f32 v157, v81, v85, s5
	v_cvt_scalef32_pk_fp8_f32 v161, v82, v86, s5
	v_cvt_scalef32_pk_fp8_f32 v165, v83, v87, s5
	v_cvt_scalef32_pk_fp8_f32 v154, v96, v100, s5
	v_cvt_scalef32_pk_fp8_f32 v158, v97, v101, s5
	v_cvt_scalef32_pk_fp8_f32 v162, v98, v102, s5
	v_cvt_scalef32_pk_fp8_f32 v166, v99, v103, s5
	v_cvt_scalef32_pk_fp8_f32 v155, v112, v116, s5
	v_cvt_scalef32_pk_fp8_f32 v159, v113, v117, s5
	v_cvt_scalef32_pk_fp8_f32 v163, v114, v118, s5
	v_cvt_scalef32_pk_fp8_f32 v167, v115, v119, s5
	v_cvt_scalef32_pk_fp8_f32 v152, v72, v76, s5 op_sel:[0,0,0,1]
	v_cvt_scalef32_pk_fp8_f32 v156, v73, v77, s5 op_sel:[0,0,0,1]
	v_cvt_scalef32_pk_fp8_f32 v160, v74, v78, s5 op_sel:[0,0,0,1]
	v_cvt_scalef32_pk_fp8_f32 v164, v75, v79, s5 op_sel:[0,0,0,1]
	v_cvt_scalef32_pk_fp8_f32 v153, v88, v92, s5 op_sel:[0,0,0,1]
	v_cvt_scalef32_pk_fp8_f32 v157, v89, v93, s5 op_sel:[0,0,0,1]
	v_cvt_scalef32_pk_fp8_f32 v161, v90, v94, s5 op_sel:[0,0,0,1]
	v_cvt_scalef32_pk_fp8_f32 v165, v91, v95, s5 op_sel:[0,0,0,1]
	v_cvt_scalef32_pk_fp8_f32 v154, v104, v108, s5 op_sel:[0,0,0,1]
	v_cvt_scalef32_pk_fp8_f32 v158, v105, v109, s5 op_sel:[0,0,0,1]
	v_cvt_scalef32_pk_fp8_f32 v162, v106, v110, s5 op_sel:[0,0,0,1]
	v_cvt_scalef32_pk_fp8_f32 v166, v107, v111, s5 op_sel:[0,0,0,1]
	v_cvt_scalef32_pk_fp8_f32 v155, v120, v124, s5 op_sel:[0,0,0,1]
	v_cvt_scalef32_pk_fp8_f32 v159, v121, v125, s5 op_sel:[0,0,0,1]
	v_cvt_scalef32_pk_fp8_f32 v163, v122, v126, s5 op_sel:[0,0,0,1]
	v_cvt_scalef32_pk_fp8_f32 v167, v123, v127, s5 op_sel:[0,0,0,1]
	s_add_u32 s100, s100, s88
	s_addc_u32 s101, s101, 0
	global_load_dwordx4 v[64:67], v132, s[100:101] nt
	global_load_dwordx4 v[68:71], v133, s[100:101] nt
	global_load_dwordx4 v[72:75], v134, s[100:101] nt
	global_load_dwordx4 v[76:79], v135, s[100:101] nt
	global_load_dwordx4 v[80:83], v136, s[100:101] nt
	global_load_dwordx4 v[84:87], v137, s[100:101] nt
	global_load_dwordx4 v[88:91], v138, s[100:101] nt
	global_load_dwordx4 v[92:95], v139, s[100:101] nt
	global_load_dwordx4 v[96:99], v140, s[100:101] nt
	global_load_dwordx4 v[100:103], v141, s[100:101] nt
	global_load_dwordx4 v[104:107], v142, s[100:101] nt
	global_load_dwordx4 v[108:111], v143, s[100:101] nt
	global_load_dwordx4 v[112:115], v144, s[100:101] nt
	global_load_dwordx4 v[116:119], v145, s[100:101] nt
	global_load_dwordx4 v[120:123], v146, s[100:101] nt
	global_load_dwordx4 v[124:127], v147, s[100:101] nt
	ds_write_b128 v148, v[152:155] offset:32768
	ds_write_b128 v148, v[156:159] offset:32896
	ds_write_b128 v149, v[160:163] offset:32768
	ds_write_b128 v149, v[164:167] offset:32896
	s_waitcnt lgkmcnt(0)
	s_barrier
; #define G_SCHED __builtin_amdgcn_sched_barrier(0)
; #define CI_LOAD(R, kt) do { _Pragma("unroll") for (int _j = 0; _j < 16; ++_j) R[_j] = __builtin_nontemporal_load((const f32x4*)(src + (size_t)((kt) * 128 + _j) * LDB)); } while (0)
; template <int LDB>
; __device__ __forceinline__ void convert_image(const float* __restrict__ W, int col0, int col1, unsigned char* __restrict__ img, LAS3 char* lds, int wid) {
;     ...
;     f32x4 ra[16], rb[16];
;     CI_LOAD(ra, 0);
;     for (int kt = 0; kt < 16; kt += 2) {
;         CI_LOAD(rb, kt + 1); G_SCHED;
;         CI_CONV(ra, kt); G_SCHED;
;         CI_LOAD(ra, (kt + 2 < 16) ? kt + 2 : 15); G_SCHED;
;         CI_CONV(rb, kt + 1); G_SCHED;
;     }
	ds_read_b128 v[168:171], v150 offset:32768
	ds_read_b128 v[172:175], v150 offset:33792
	ds_read_b128 v[176:179], v150 offset:34816
	ds_read_b128 v[180:183], v150 offset:35840
	s_waitcnt lgkmcnt(3)
	global_store_dwordx4 v150, v[168:171], s[6:7] sc1
	s_waitcnt lgkmcnt(2)
	global_store_dwordx4 v150, v[172:175], s[6:7] offset:1024 sc1
	s_waitcnt lgkmcnt(1)
	global_store_dwordx4 v150, v[176:179], s[6:7] offset:2048 sc1
	s_waitcnt lgkmcnt(0)
	global_store_dwordx4 v150, v[180:183], s[6:7] offset:3072 sc1
	s_add_u32 s6, s6, 0x8000
	s_addc_u32 s7, s7, 0
	s_waitcnt vmcnt(40)
	v_cvt_scalef32_pk_fp8_f32 v152, v184, v188, s5
	v_cvt_scalef32_pk_fp8_f32 v156, v185, v189, s5
	v_cvt_scalef32_pk_fp8_f32 v160, v186, v190, s5
	v_cvt_scalef32_pk_fp8_f32 v164, v187, v191, s5
	v_cvt_scalef32_pk_fp8_f32 v153, v200, v204, s5
	v_cvt_scalef32_pk_fp8_f32 v157, v201, v205, s5
	v_cvt_scalef32_pk_fp8_f32 v161, v202, v206, s5
	v_cvt_scalef32_pk_fp8_f32 v165, v203, v207, s5
	v_cvt_scalef32_pk_fp8_f32 v154, v216, v220, s5
	v_cvt_scalef32_pk_fp8_f32 v158, v217, v221, s5
	v_cvt_scalef32_pk_fp8_f32 v162, v218, v222, s5
	v_cvt_scalef32_pk_fp8_f32 v166, v219, v223, s5
	v_cvt_scalef32_pk_fp8_f32 v155, v232, v236, s5
	v_cvt_scalef32_pk_fp8_f32 v159, v233, v237, s5
	v_cvt_scalef32_pk_fp8_f32 v163, v234, v238, s5
	v_cvt_scalef32_pk_fp8_f32 v167, v235, v239, s5
	v_cvt_scalef32_pk_fp8_f32 v152, v192, v196, s5 op_sel:[0,0,0,1]
	v_cvt_scalef32_pk_fp8_f32 v156, v193, v197, s5 op_sel:[0,0,0,1]
	v_cvt_scalef32_pk_fp8_f32 v160, v194, v198, s5 op_sel:[0,0,0,1]
	v_cvt_scalef32_pk_fp8_f32 v164, v195, v199, s5 op_sel:[0,0,0,1]
	v_cvt_scalef32_pk_fp8_f32 v153, v208, v212, s5 op_sel:[0,0,0,1]
	v_cvt_scalef32_pk_fp8_f32 v157, v209, v213, s5 op_sel:[0,0,0,1]
	v_cvt_scalef32_pk_fp8_f32 v161, v210, v214, s5 op_sel:[0,0,0,1]
	v_cvt_scalef32_pk_fp8_f32 v165, v211, v215, s5 op_sel:[0,0,0,1]
	v_cvt_scalef32_pk_fp8_f32 v154, v224, v228, s5 op_sel:[0,0,0,1]
	v_cvt_scalef32_pk_fp8_f32 v158, v225, v229, s5 op_sel:[0,0,0,1]
	v_cvt_scalef32_pk_fp8_f32 v162, v226, v230, s5 op_sel:[0,0,0,1]
	v_cvt_scalef32_pk_fp8_f32 v166, v227, v231, s5 op_sel:[0,0,0,1]
	v_cvt_scalef32_pk_fp8_f32 v155, v240, v244, s5 op_sel:[0,0,0,1]
	v_cvt_scalef32_pk_fp8_f32 v159, v241, v245, s5 op_sel:[0,0,0,1]
	v_cvt_scalef32_pk_fp8_f32 v163, v242, v246, s5 op_sel:[0,0,0,1]
	v_cvt_scalef32_pk_fp8_f32 v167, v243, v247, s5 op_sel:[0,0,0,1]
	s_add_u32 s100, s100, s88
	s_addc_u32 s101, s101, 0
	global_load_dwordx4 v[184:187], v132, s[100:101] nt
	global_load_dwordx4 v[188:191], v133, s[100:101] nt
	global_load_dwordx4 v[192:195], v134, s[100:101] nt
	global_load_dwordx4 v[196:199], v135, s[100:101] nt
	global_load_dwordx4 v[200:203], v136, s[100:101] nt
	global_load_dwordx4 v[204:207], v137, s[100:101] nt
	global_load_dwordx4 v[208:211], v138, s[100:101] nt
	global_load_dwordx4 v[212:215], v139, s[100:101] nt
	global_load_dwordx4 v[216:219], v140, s[100:101] nt
	global_load_dwordx4 v[220:223], v141, s[100:101] nt
	global_load_dwordx4 v[224:227], v142, s[100:101] nt
	global_load_dwordx4 v[228:231], v143, s[100:101] nt
	global_load_dwordx4 v[232:235], v144, s[100:101] nt
	global_load_dwordx4 v[236:239], v145, s[100:101] nt
	global_load_dwordx4 v[240:243], v146, s[100:101] nt
	global_load_dwordx4 v[244:247], v147, s[100:101] nt
	ds_write_b128 v148, v[152:155] offset:0
	ds_write_b128 v148, v[156:159] offset:128
	ds_write_b128 v149, v[160:163] offset:0
	ds_write_b128 v149, v[164:167] offset:128
	s_waitcnt lgkmcnt(0)
	s_barrier
	ds_read_b128 v[168:171], v150 offset:0
	ds_read_b128 v[172:175], v150 offset:1024
	ds_read_b128 v[176:179], v150 offset:2048
	ds_read_b128 v[180:183], v150 offset:3072
	s_waitcnt lgkmcnt(3)
	global_store_dwordx4 v150, v[168:171], s[6:7] sc1
	s_waitcnt lgkmcnt(2)
	global_store_dwordx4 v150, v[172:175], s[6:7] offset:1024 sc1
	s_waitcnt lgkmcnt(1)
	global_store_dwordx4 v150, v[176:179], s[6:7] offset:2048 sc1
	s_waitcnt lgkmcnt(0)
	global_store_dwordx4 v150, v[180:183], s[6:7] offset:3072 sc1
	s_add_u32 s6, s6, 0x8000
	s_addc_u32 s7, s7, 0
	s_waitcnt vmcnt(44)
	v_cvt_scalef32_pk_fp8_f32 v152, v0, v4, s5
	v_cvt_scalef32_pk_fp8_f32 v156, v1, v5, s5
	v_cvt_scalef32_pk_fp8_f32 v160, v2, v6, s5
	v_cvt_scalef32_pk_fp8_f32 v164, v3, v7, s5
	v_cvt_scalef32_pk_fp8_f32 v153, v16, v20, s5
	v_cvt_scalef32_pk_fp8_f32 v157, v17, v21, s5
	v_cvt_scalef32_pk_fp8_f32 v161, v18, v22, s5
	v_cvt_scalef32_pk_fp8_f32 v165, v19, v23, s5
	v_cvt_scalef32_pk_fp8_f32 v154, v32, v36, s5
	v_cvt_scalef32_pk_fp8_f32 v158, v33, v37, s5
	v_cvt_scalef32_pk_fp8_f32 v162, v34, v38, s5
	v_cvt_scalef32_pk_fp8_f32 v166, v35, v39, s5
	v_cvt_scalef32_pk_fp8_f32 v155, v48, v52, s5
	v_cvt_scalef32_pk_fp8_f32 v159, v49, v53, s5
	v_cvt_scalef32_pk_fp8_f32 v163, v50, v54, s5
	v_cvt_scalef32_pk_fp8_f32 v167, v51, v55, s5
	v_cvt_scalef32_pk_fp8_f32 v152, v8, v12, s5 op_sel:[0,0,0,1]
	v_cvt_scalef32_pk_fp8_f32 v156, v9, v13, s5 op_sel:[0,0,0,1]
	v_cvt_scalef32_pk_fp8_f32 v160, v10, v14, s5 op_sel:[0,0,0,1]
	v_cvt_scalef32_pk_fp8_f32 v164, v11, v15, s5 op_sel:[0,0,0,1]
	v_cvt_scalef32_pk_fp8_f32 v153, v24, v28, s5 op_sel:[0,0,0,1]
	v_cvt_scalef32_pk_fp8_f32 v157, v25, v29, s5 op_sel:[0,0,0,1]
	v_cvt_scalef32_pk_fp8_f32 v161, v26, v30, s5 op_sel:[0,0,0,1]
	v_cvt_scalef32_pk_fp8_f32 v165, v27, v31, s5 op_sel:[0,0,0,1]
	v_cvt_scalef32_pk_fp8_f32 v154, v40, v44, s5 op_sel:[0,0,0,1]
	v_cvt_scalef32_pk_fp8_f32 v158, v41, v45, s5 op_sel:[0,0,0,1]
	v_cvt_scalef32_pk_fp8_f32 v162, v42, v46, s5 op_sel:[0,0,0,1]
	v_cvt_scalef32_pk_fp8_f32 v166, v43, v47, s5 op_sel:[0,0,0,1]
	v_cvt_scalef32_pk_fp8_f32 v155, v56, v60, s5 op_sel:[0,0,0,1]
	v_cvt_scalef32_pk_fp8_f32 v159, v57, v61, s5 op_sel:[0,0,0,1]
	v_cvt_scalef32_pk_fp8_f32 v163, v58, v62, s5 op_sel:[0,0,0,1]
	v_cvt_scalef32_pk_fp8_f32 v167, v59, v63, s5 op_sel:[0,0,0,1]
	s_add_u32 s100, s100, s88
	s_addc_u32 s101, s101, 0
	global_load_dwordx4 v[0:3], v132, s[100:101] nt
	global_load_dwordx4 v[4:7], v133, s[100:101] nt
	global_load_dwordx4 v[8:11], v134, s[100:101] nt
	global_load_dwordx4 v[12:15], v135, s[100:101] nt
	global_load_dwordx4 v[16:19], v136, s[100:101] nt
	global_load_dwordx4 v[20:23], v137, s[100:101] nt
	global_load_dwordx4 v[24:27], v138, s[100:101] nt
	global_load_dwordx4 v[28:31], v139, s[100:101] nt
	global_load_dwordx4 v[32:35], v140, s[100:101] nt
	global_load_dwordx4 v[36:39], v141, s[100:101] nt
	global_load_dwordx4 v[40:43], v142, s[100:101] nt
	global_load_dwordx4 v[44:47], v143, s[100:101] nt
	global_load_dwordx4 v[48:51], v144, s[100:101] nt
	global_load_dwordx4 v[52:55], v145, s[100:101] nt
	global_load_dwordx4 v[56:59], v146, s[100:101] nt
	global_load_dwordx4 v[60:63], v147, s[100:101] nt
	ds_write_b128 v148, v[152:155] offset:32768
	ds_write_b128 v148, v[156:159] offset:32896
	ds_write_b128 v149, v[160:163] offset:32768
	ds_write_b128 v149, v[164:167] offset:32896
	s_waitcnt lgkmcnt(0)
	s_barrier
; #define G_SCHED __builtin_amdgcn_sched_barrier(0)
; #define CI_LOAD(R, kt) do { _Pragma("unroll") for (int _j = 0; _j < 16; ++_j) R[_j] = __builtin_nontemporal_load((const f32x4*)(src + (size_t)((kt) * 128 + _j) * LDB)); } while (0)
; template <int LDB>
; __device__ __forceinline__ void convert_image(const float* __restrict__ W, int col0, int col1, unsigned char* __restrict__ img, LAS3 char* lds, int wid) {
;     ...
;     f32x4 ra[16], rb[16];
;     CI_LOAD(ra, 0);
;     for (int kt = 0; kt < 16; kt += 2) {
;         CI_LOAD(rb, kt + 1); G_SCHED;
;         CI_CONV(ra, kt); G_SCHED;
;         CI_LOAD(ra, (kt + 2 < 16) ? kt + 2 : 15); G_SCHED;
;         CI_CONV(rb, kt + 1); G_SCHED;
;     }
	ds_read_b128 v[168:171], v150 offset:32768
	ds_read_b128 v[172:175], v150 offset:33792
	ds_read_b128 v[176:179], v150 offset:34816
	ds_read_b128 v[180:183], v150 offset:35840
	s_waitcnt lgkmcnt(3)
	global_store_dwordx4 v150, v[168:171], s[6:7] sc1
	s_waitcnt lgkmcnt(2)
	global_store_dwordx4 v150, v[172:175], s[6:7] offset:1024 sc1
	s_waitcnt lgkmcnt(1)
	global_store_dwordx4 v150, v[176:179], s[6:7] offset:2048 sc1
	s_waitcnt lgkmcnt(0)
	global_store_dwordx4 v150, v[180:183], s[6:7] offset:3072 sc1
	s_add_u32 s6, s6, 0x8000
	s_addc_u32 s7, s7, 0
	s_waitcnt vmcnt(44)
	v_cvt_scalef32_pk_fp8_f32 v152, v64, v68, s5
	v_cvt_scalef32_pk_fp8_f32 v156, v65, v69, s5
	v_cvt_scalef32_pk_fp8_f32 v160, v66, v70, s5
	v_cvt_scalef32_pk_fp8_f32 v164, v67, v71, s5
	v_cvt_scalef32_pk_fp8_f32 v153, v80, v84, s5
	v_cvt_scalef32_pk_fp8_f32 v157, v81, v85, s5
	v_cvt_scalef32_pk_fp8_f32 v161, v82, v86, s5
	v_cvt_scalef32_pk_fp8_f32 v165, v83, v87, s5
	v_cvt_scalef32_pk_fp8_f32 v154, v96, v100, s5
	v_cvt_scalef32_pk_fp8_f32 v158, v97, v101, s5
	v_cvt_scalef32_pk_fp8_f32 v162, v98, v102, s5
	v_cvt_scalef32_pk_fp8_f32 v166, v99, v103, s5
	v_cvt_scalef32_pk_fp8_f32 v155, v112, v116, s5
	v_cvt_scalef32_pk_fp8_f32 v159, v113, v117, s5
	v_cvt_scalef32_pk_fp8_f32 v163, v114, v118, s5
	v_cvt_scalef32_pk_fp8_f32 v167, v115, v119, s5
	v_cvt_scalef32_pk_fp8_f32 v152, v72, v76, s5 op_sel:[0,0,0,1]
	v_cvt_scalef32_pk_fp8_f32 v156, v73, v77, s5 op_sel:[0,0,0,1]
	v_cvt_scalef32_pk_fp8_f32 v160, v74, v78, s5 op_sel:[0,0,0,1]
	v_cvt_scalef32_pk_fp8_f32 v164, v75, v79, s5 op_sel:[0,0,0,1]
	v_cvt_scalef32_pk_fp8_f32 v153, v88, v92, s5 op_sel:[0,0,0,1]
	v_cvt_scalef32_pk_fp8_f32 v157, v89, v93, s5 op_sel:[0,0,0,1]
	v_cvt_scalef32_pk_fp8_f32 v161, v90, v94, s5 op_sel:[0,0,0,1]
	v_cvt_scalef32_pk_fp8_f32 v165, v91, v95, s5 op_sel:[0,0,0,1]
	v_cvt_scalef32_pk_fp8_f32 v154, v104, v108, s5 op_sel:[0,0,0,1]
	v_cvt_scalef32_pk_fp8_f32 v158, v105, v109, s5 op_sel:[0,0,0,1]
	v_cvt_scalef32_pk_fp8_f32 v162, v106, v110, s5 op_sel:[0,0,0,1]
	v_cvt_scalef32_pk_fp8_f32 v166, v107, v111, s5 op_sel:[0,0,0,1]
	v_cvt_scalef32_pk_fp8_f32 v155, v120, v124, s5 op_sel:[0,0,0,1]
	v_cvt_scalef32_pk_fp8_f32 v159, v121, v125, s5 op_sel:[0,0,0,1]
	v_cvt_scalef32_pk_fp8_f32 v163, v122, v126, s5 op_sel:[0,0,0,1]
	v_cvt_scalef32_pk_fp8_f32 v167, v123, v127, s5 op_sel:[0,0,0,1]
	s_add_u32 s100, s100, s88
	s_addc_u32 s101, s101, 0
	global_load_dwordx4 v[64:67], v132, s[100:101] nt
	global_load_dwordx4 v[68:71], v133, s[100:101] nt
	global_load_dwordx4 v[72:75], v134, s[100:101] nt
	global_load_dwordx4 v[76:79], v135, s[100:101] nt
	global_load_dwordx4 v[80:83], v136, s[100:101] nt
	global_load_dwordx4 v[84:87], v137, s[100:101] nt
	global_load_dwordx4 v[88:91], v138, s[100:101] nt
	global_load_dwordx4 v[92:95], v139, s[100:101] nt
	global_load_dwordx4 v[96:99], v140, s[100:101] nt
	global_load_dwordx4 v[100:103], v141, s[100:101] nt
	global_load_dwordx4 v[104:107], v142, s[100:101] nt
	global_load_dwordx4 v[108:111], v143, s[100:101] nt
	global_load_dwordx4 v[112:115], v144, s[100:101] nt
	global_load_dwordx4 v[116:119], v145, s[100:101] nt
	global_load_dwordx4 v[120:123], v146, s[100:101] nt
	global_load_dwordx4 v[124:127], v147, s[100:101] nt
	ds_write_b128 v148, v[152:155] offset:0
	ds_write_b128 v148, v[156:159] offset:128
	ds_write_b128 v149, v[160:163] offset:0
	ds_write_b128 v149, v[164:167] offset:128
	s_waitcnt lgkmcnt(0)
	s_barrier
	ds_read_b128 v[168:171], v150 offset:0
	ds_read_b128 v[172:175], v150 offset:1024
	ds_read_b128 v[176:179], v150 offset:2048
	ds_read_b128 v[180:183], v150 offset:3072
	s_waitcnt lgkmcnt(3)
	global_store_dwordx4 v150, v[168:171], s[6:7] sc1
	s_waitcnt lgkmcnt(2)
	global_store_dwordx4 v150, v[172:175], s[6:7] offset:1024 sc1
	s_waitcnt lgkmcnt(1)
	global_store_dwordx4 v150, v[176:179], s[6:7] offset:2048 sc1
	s_waitcnt lgkmcnt(0)
	global_store_dwordx4 v150, v[180:183], s[6:7] offset:3072 sc1
	s_add_u32 s6, s6, 0x8000
	s_addc_u32 s7, s7, 0
	s_waitcnt vmcnt(44)
	v_cvt_scalef32_pk_fp8_f32 v152, v184, v188, s5
	v_cvt_scalef32_pk_fp8_f32 v156, v185, v189, s5
	v_cvt_scalef32_pk_fp8_f32 v160, v186, v190, s5
	v_cvt_scalef32_pk_fp8_f32 v164, v187, v191, s5
	v_cvt_scalef32_pk_fp8_f32 v153, v200, v204, s5
	v_cvt_scalef32_pk_fp8_f32 v157, v201, v205, s5
	v_cvt_scalef32_pk_fp8_f32 v161, v202, v206, s5
	v_cvt_scalef32_pk_fp8_f32 v165, v203, v207, s5
	v_cvt_scalef32_pk_fp8_f32 v154, v216, v220, s5
	v_cvt_scalef32_pk_fp8_f32 v158, v217, v221, s5
	v_cvt_scalef32_pk_fp8_f32 v162, v218, v222, s5
	v_cvt_scalef32_pk_fp8_f32 v166, v219, v223, s5
	v_cvt_scalef32_pk_fp8_f32 v155, v232, v236, s5
	v_cvt_scalef32_pk_fp8_f32 v159, v233, v237, s5
	v_cvt_scalef32_pk_fp8_f32 v163, v234, v238, s5
	v_cvt_scalef32_pk_fp8_f32 v167, v235, v239, s5
	v_cvt_scalef32_pk_fp8_f32 v152, v192, v196, s5 op_sel:[0,0,0,1]
	v_cvt_scalef32_pk_fp8_f32 v156, v193, v197, s5 op_sel:[0,0,0,1]
	v_cvt_scalef32_pk_fp8_f32 v160, v194, v198, s5 op_sel:[0,0,0,1]
	v_cvt_scalef32_pk_fp8_f32 v164, v195, v199, s5 op_sel:[0,0,0,1]
	v_cvt_scalef32_pk_fp8_f32 v153, v208, v212, s5 op_sel:[0,0,0,1]
	v_cvt_scalef32_pk_fp8_f32 v157, v209, v213, s5 op_sel:[0,0,0,1]
	v_cvt_scalef32_pk_fp8_f32 v161, v210, v214, s5 op_sel:[0,0,0,1]
	v_cvt_scalef32_pk_fp8_f32 v165, v211, v215, s5 op_sel:[0,0,0,1]
	v_cvt_scalef32_pk_fp8_f32 v154, v224, v228, s5 op_sel:[0,0,0,1]
	v_cvt_scalef32_pk_fp8_f32 v158, v225, v229, s5 op_sel:[0,0,0,1]
	v_cvt_scalef32_pk_fp8_f32 v162, v226, v230, s5 op_sel:[0,0,0,1]
	v_cvt_scalef32_pk_fp8_f32 v166, v227, v231, s5 op_sel:[0,0,0,1]
	v_cvt_scalef32_pk_fp8_f32 v155, v240, v244, s5 op_sel:[0,0,0,1]
	v_cvt_scalef32_pk_fp8_f32 v159, v241, v245, s5 op_sel:[0,0,0,1]
	v_cvt_scalef32_pk_fp8_f32 v163, v242, v246, s5 op_sel:[0,0,0,1]
	v_cvt_scalef32_pk_fp8_f32 v167, v243, v247, s5 op_sel:[0,0,0,1]
	s_add_u32 s100, s100, s88
	s_addc_u32 s101, s101, 0
	global_load_dwordx4 v[184:187], v132, s[100:101] nt
	global_load_dwordx4 v[188:191], v133, s[100:101] nt
	global_load_dwordx4 v[192:195], v134, s[100:101] nt
	global_load_dwordx4 v[196:199], v135, s[100:101] nt
	global_load_dwordx4 v[200:203], v136, s[100:101] nt
	global_load_dwordx4 v[204:207], v137, s[100:101] nt
	global_load_dwordx4 v[208:211], v138, s[100:101] nt
	global_load_dwordx4 v[212:215], v139, s[100:101] nt
	global_load_dwordx4 v[216:219], v140, s[100:101] nt
	global_load_dwordx4 v[220:223], v141, s[100:101] nt
	global_load_dwordx4 v[224:227], v142, s[100:101] nt
	global_load_dwordx4 v[228:231], v143, s[100:101] nt
	global_load_dwordx4 v[232:235], v144, s[100:101] nt
	global_load_dwordx4 v[236:239], v145, s[100:101] nt
	global_load_dwordx4 v[240:243], v146, s[100:101] nt
	global_load_dwordx4 v[244:247], v147, s[100:101] nt
	ds_write_b128 v148, v[152:155] offset:32768
	ds_write_b128 v148, v[156:159] offset:32896
	ds_write_b128 v149, v[160:163] offset:32768
	ds_write_b128 v149, v[164:167] offset:32896
	s_waitcnt lgkmcnt(0)
	s_barrier
; #define G_SCHED __builtin_amdgcn_sched_barrier(0)
; #define CI_LOAD(R, kt) do { _Pragma("unroll") for (int _j = 0; _j < 16; ++_j) R[_j] = __builtin_nontemporal_load((const f32x4*)(src + (size_t)((kt) * 128 + _j) * LDB)); } while (0)
; template <int LDB>
; __device__ __forceinline__ void convert_image(const float* __restrict__ W, int col0, int col1, unsigned char* __restrict__ img, LAS3 char* lds, int wid) {
;     ...
;     f32x4 ra[16], rb[16];
;     CI_LOAD(ra, 0);
;     for (int kt = 0; kt < 16; kt += 2) {
;         CI_LOAD(rb, kt + 1); G_SCHED;
;         CI_CONV(ra, kt); G_SCHED;
;         CI_LOAD(ra, (kt + 2 < 16) ? kt + 2 : 15); G_SCHED;
;         CI_CONV(rb, kt + 1); G_SCHED;
;     }
	ds_read_b128 v[168:171], v150 offset:32768
	ds_read_b128 v[172:175], v150 offset:33792
	ds_read_b128 v[176:179], v150 offset:34816
	ds_read_b128 v[180:183], v150 offset:35840
	s_waitcnt lgkmcnt(3)
	global_store_dwordx4 v150, v[168:171], s[6:7] sc1
	s_waitcnt lgkmcnt(2)
	global_store_dwordx4 v150, v[172:175], s[6:7] offset:1024 sc1
	s_waitcnt lgkmcnt(1)
	global_store_dwordx4 v150, v[176:179], s[6:7] offset:2048 sc1
	s_waitcnt lgkmcnt(0)
	global_store_dwordx4 v150, v[180:183], s[6:7] offset:3072 sc1
	s_add_u32 s6, s6, 0x8000
	s_addc_u32 s7, s7, 0
	s_waitcnt vmcnt(44)
	v_cvt_scalef32_pk_fp8_f32 v152, v0, v4, s5
	v_cvt_scalef32_pk_fp8_f32 v156, v1, v5, s5
	v_cvt_scalef32_pk_fp8_f32 v160, v2, v6, s5
	v_cvt_scalef32_pk_fp8_f32 v164, v3, v7, s5
	v_cvt_scalef32_pk_fp8_f32 v153, v16, v20, s5
	v_cvt_scalef32_pk_fp8_f32 v157, v17, v21, s5
	v_cvt_scalef32_pk_fp8_f32 v161, v18, v22, s5
	v_cvt_scalef32_pk_fp8_f32 v165, v19, v23, s5
	v_cvt_scalef32_pk_fp8_f32 v154, v32, v36, s5
	v_cvt_scalef32_pk_fp8_f32 v158, v33, v37, s5
	v_cvt_scalef32_pk_fp8_f32 v162, v34, v38, s5
	v_cvt_scalef32_pk_fp8_f32 v166, v35, v39, s5
	v_cvt_scalef32_pk_fp8_f32 v155, v48, v52, s5
	v_cvt_scalef32_pk_fp8_f32 v159, v49, v53, s5
	v_cvt_scalef32_pk_fp8_f32 v163, v50, v54, s5
	v_cvt_scalef32_pk_fp8_f32 v167, v51, v55, s5
	v_cvt_scalef32_pk_fp8_f32 v152, v8, v12, s5 op_sel:[0,0,0,1]
	v_cvt_scalef32_pk_fp8_f32 v156, v9, v13, s5 op_sel:[0,0,0,1]
	v_cvt_scalef32_pk_fp8_f32 v160, v10, v14, s5 op_sel:[0,0,0,1]
	v_cvt_scalef32_pk_fp8_f32 v164, v11, v15, s5 op_sel:[0,0,0,1]
	v_cvt_scalef32_pk_fp8_f32 v153, v24, v28, s5 op_sel:[0,0,0,1]
	v_cvt_scalef32_pk_fp8_f32 v157, v25, v29, s5 op_sel:[0,0,0,1]
	v_cvt_scalef32_pk_fp8_f32 v161, v26, v30, s5 op_sel:[0,0,0,1]
	v_cvt_scalef32_pk_fp8_f32 v165, v27, v31, s5 op_sel:[0,0,0,1]
	v_cvt_scalef32_pk_fp8_f32 v154, v40, v44, s5 op_sel:[0,0,0,1]
	v_cvt_scalef32_pk_fp8_f32 v158, v41, v45, s5 op_sel:[0,0,0,1]
	v_cvt_scalef32_pk_fp8_f32 v162, v42, v46, s5 op_sel:[0,0,0,1]
	v_cvt_scalef32_pk_fp8_f32 v166, v43, v47, s5 op_sel:[0,0,0,1]
	v_cvt_scalef32_pk_fp8_f32 v155, v56, v60, s5 op_sel:[0,0,0,1]
	v_cvt_scalef32_pk_fp8_f32 v159, v57, v61, s5 op_sel:[0,0,0,1]
	v_cvt_scalef32_pk_fp8_f32 v163, v58, v62, s5 op_sel:[0,0,0,1]
	v_cvt_scalef32_pk_fp8_f32 v167, v59, v63, s5 op_sel:[0,0,0,1]
	s_add_u32 s100, s100, s88
	s_addc_u32 s101, s101, 0
	global_load_dwordx4 v[0:3], v132, s[100:101] nt
	global_load_dwordx4 v[4:7], v133, s[100:101] nt
	global_load_dwordx4 v[8:11], v134, s[100:101] nt
	global_load_dwordx4 v[12:15], v135, s[100:101] nt
	global_load_dwordx4 v[16:19], v136, s[100:101] nt
	global_load_dwordx4 v[20:23], v137, s[100:101] nt
	global_load_dwordx4 v[24:27], v138, s[100:101] nt
	global_load_dwordx4 v[28:31], v139, s[100:101] nt
	global_load_dwordx4 v[32:35], v140, s[100:101] nt
	global_load_dwordx4 v[36:39], v141, s[100:101] nt
	global_load_dwordx4 v[40:43], v142, s[100:101] nt
	global_load_dwordx4 v[44:47], v143, s[100:101] nt
	global_load_dwordx4 v[48:51], v144, s[100:101] nt
	global_load_dwordx4 v[52:55], v145, s[100:101] nt
	global_load_dwordx4 v[56:59], v146, s[100:101] nt
	global_load_dwordx4 v[60:63], v147, s[100:101] nt
	ds_write_b128 v148, v[152:155] offset:0
	ds_write_b128 v148, v[156:159] offset:128
	ds_write_b128 v149, v[160:163] offset:0
	ds_write_b128 v149, v[164:167] offset:128
	s_waitcnt lgkmcnt(0)
	s_barrier
	ds_read_b128 v[168:171], v150 offset:0
	ds_read_b128 v[172:175], v150 offset:1024
	ds_read_b128 v[176:179], v150 offset:2048
	ds_read_b128 v[180:183], v150 offset:3072
	s_waitcnt lgkmcnt(3)
	global_store_dwordx4 v150, v[168:171], s[6:7] sc1
	s_waitcnt lgkmcnt(2)
	global_store_dwordx4 v150, v[172:175], s[6:7] offset:1024 sc1
	s_waitcnt lgkmcnt(1)
	global_store_dwordx4 v150, v[176:179], s[6:7] offset:2048 sc1
	s_waitcnt lgkmcnt(0)
	global_store_dwordx4 v150, v[180:183], s[6:7] offset:3072 sc1
	s_add_u32 s6, s6, 0x8000
	s_addc_u32 s7, s7, 0
	s_waitcnt vmcnt(44)
	v_cvt_scalef32_pk_fp8_f32 v152, v64, v68, s5
	v_cvt_scalef32_pk_fp8_f32 v156, v65, v69, s5
	v_cvt_scalef32_pk_fp8_f32 v160, v66, v70, s5
	v_cvt_scalef32_pk_fp8_f32 v164, v67, v71, s5
	v_cvt_scalef32_pk_fp8_f32 v153, v80, v84, s5
	v_cvt_scalef32_pk_fp8_f32 v157, v81, v85, s5
	v_cvt_scalef32_pk_fp8_f32 v161, v82, v86, s5
	v_cvt_scalef32_pk_fp8_f32 v165, v83, v87, s5
	v_cvt_scalef32_pk_fp8_f32 v154, v96, v100, s5
	v_cvt_scalef32_pk_fp8_f32 v158, v97, v101, s5
	v_cvt_scalef32_pk_fp8_f32 v162, v98, v102, s5
	v_cvt_scalef32_pk_fp8_f32 v166, v99, v103, s5
	v_cvt_scalef32_pk_fp8_f32 v155, v112, v116, s5
	v_cvt_scalef32_pk_fp8_f32 v159, v113, v117, s5
	v_cvt_scalef32_pk_fp8_f32 v163, v114, v118, s5
	v_cvt_scalef32_pk_fp8_f32 v167, v115, v119, s5
	v_cvt_scalef32_pk_fp8_f32 v152, v72, v76, s5 op_sel:[0,0,0,1]
	v_cvt_scalef32_pk_fp8_f32 v156, v73, v77, s5 op_sel:[0,0,0,1]
	v_cvt_scalef32_pk_fp8_f32 v160, v74, v78, s5 op_sel:[0,0,0,1]
	v_cvt_scalef32_pk_fp8_f32 v164, v75, v79, s5 op_sel:[0,0,0,1]
	v_cvt_scalef32_pk_fp8_f32 v153, v88, v92, s5 op_sel:[0,0,0,1]
	v_cvt_scalef32_pk_fp8_f32 v157, v89, v93, s5 op_sel:[0,0,0,1]
	v_cvt_scalef32_pk_fp8_f32 v161, v90, v94, s5 op_sel:[0,0,0,1]
	v_cvt_scalef32_pk_fp8_f32 v165, v91, v95, s5 op_sel:[0,0,0,1]
	v_cvt_scalef32_pk_fp8_f32 v154, v104, v108, s5 op_sel:[0,0,0,1]
	v_cvt_scalef32_pk_fp8_f32 v158, v105, v109, s5 op_sel:[0,0,0,1]
	v_cvt_scalef32_pk_fp8_f32 v162, v106, v110, s5 op_sel:[0,0,0,1]
	v_cvt_scalef32_pk_fp8_f32 v166, v107, v111, s5 op_sel:[0,0,0,1]
	v_cvt_scalef32_pk_fp8_f32 v155, v120, v124, s5 op_sel:[0,0,0,1]
	v_cvt_scalef32_pk_fp8_f32 v159, v121, v125, s5 op_sel:[0,0,0,1]
	v_cvt_scalef32_pk_fp8_f32 v163, v122, v126, s5 op_sel:[0,0,0,1]
	v_cvt_scalef32_pk_fp8_f32 v167, v123, v127, s5 op_sel:[0,0,0,1]
	s_add_u32 s100, s100, s88
	s_addc_u32 s101, s101, 0
	global_load_dwordx4 v[64:67], v132, s[100:101] nt
	global_load_dwordx4 v[68:71], v133, s[100:101] nt
	global_load_dwordx4 v[72:75], v134, s[100:101] nt
	global_load_dwordx4 v[76:79], v135, s[100:101] nt
	global_load_dwordx4 v[80:83], v136, s[100:101] nt
	global_load_dwordx4 v[84:87], v137, s[100:101] nt
	global_load_dwordx4 v[88:91], v138, s[100:101] nt
	global_load_dwordx4 v[92:95], v139, s[100:101] nt
	global_load_dwordx4 v[96:99], v140, s[100:101] nt
	global_load_dwordx4 v[100:103], v141, s[100:101] nt
	global_load_dwordx4 v[104:107], v142, s[100:101] nt
	global_load_dwordx4 v[108:111], v143, s[100:101] nt
	global_load_dwordx4 v[112:115], v144, s[100:101] nt
	global_load_dwordx4 v[116:119], v145, s[100:101] nt
	global_load_dwordx4 v[120:123], v146, s[100:101] nt
	global_load_dwordx4 v[124:127], v147, s[100:101] nt
	ds_write_b128 v148, v[152:155] offset:32768
	ds_write_b128 v148, v[156:159] offset:32896
	ds_write_b128 v149, v[160:163] offset:32768
	ds_write_b128 v149, v[164:167] offset:32896
	s_waitcnt lgkmcnt(0)
	s_barrier
; #define G_SCHED __builtin_amdgcn_sched_barrier(0)
; #define CI_LOAD(R, kt) do { _Pragma("unroll") for (int _j = 0; _j < 16; ++_j) R[_j] = __builtin_nontemporal_load((const f32x4*)(src + (size_t)((kt) * 128 + _j) * LDB)); } while (0)
; template <int LDB>
; __device__ __forceinline__ void convert_image(const float* __restrict__ W, int col0, int col1, unsigned char* __restrict__ img, LAS3 char* lds, int wid) {
;     ...
;     f32x4 ra[16], rb[16];
;     CI_LOAD(ra, 0);
;     for (int kt = 0; kt < 16; kt += 2) {
;         CI_LOAD(rb, kt + 1); G_SCHED;
;         CI_CONV(ra, kt); G_SCHED;
;         CI_LOAD(ra, (kt + 2 < 16) ? kt + 2 : 15); G_SCHED;
;         CI_CONV(rb, kt + 1); G_SCHED;
;     }
	ds_read_b128 v[168:171], v150 offset:32768
	ds_read_b128 v[172:175], v150 offset:33792
	ds_read_b128 v[176:179], v150 offset:34816
	ds_read_b128 v[180:183], v150 offset:35840
	s_waitcnt lgkmcnt(3)
	global_store_dwordx4 v150, v[168:171], s[6:7] sc1
	s_waitcnt lgkmcnt(2)
	global_store_dwordx4 v150, v[172:175], s[6:7] offset:1024 sc1
	s_waitcnt lgkmcnt(1)
	global_store_dwordx4 v150, v[176:179], s[6:7] offset:2048 sc1
	s_waitcnt lgkmcnt(0)
	global_store_dwordx4 v150, v[180:183], s[6:7] offset:3072 sc1
	s_add_u32 s6, s6, 0x8000
	s_addc_u32 s7, s7, 0
	s_waitcnt vmcnt(44)
	v_cvt_scalef32_pk_fp8_f32 v152, v184, v188, s5
	v_cvt_scalef32_pk_fp8_f32 v156, v185, v189, s5
	v_cvt_scalef32_pk_fp8_f32 v160, v186, v190, s5
	v_cvt_scalef32_pk_fp8_f32 v164, v187, v191, s5
	v_cvt_scalef32_pk_fp8_f32 v153, v200, v204, s5
	v_cvt_scalef32_pk_fp8_f32 v157, v201, v205, s5
	v_cvt_scalef32_pk_fp8_f32 v161, v202, v206, s5
	v_cvt_scalef32_pk_fp8_f32 v165, v203, v207, s5
	v_cvt_scalef32_pk_fp8_f32 v154, v216, v220, s5
	v_cvt_scalef32_pk_fp8_f32 v158, v217, v221, s5
	v_cvt_scalef32_pk_fp8_f32 v162, v218, v222, s5
	v_cvt_scalef32_pk_fp8_f32 v166, v219, v223, s5
	v_cvt_scalef32_pk_fp8_f32 v155, v232, v236, s5
	v_cvt_scalef32_pk_fp8_f32 v159, v233, v237, s5
	v_cvt_scalef32_pk_fp8_f32 v163, v234, v238, s5
	v_cvt_scalef32_pk_fp8_f32 v167, v235, v239, s5
	v_cvt_scalef32_pk_fp8_f32 v152, v192, v196, s5 op_sel:[0,0,0,1]
	v_cvt_scalef32_pk_fp8_f32 v156, v193, v197, s5 op_sel:[0,0,0,1]
	v_cvt_scalef32_pk_fp8_f32 v160, v194, v198, s5 op_sel:[0,0,0,1]
	v_cvt_scalef32_pk_fp8_f32 v164, v195, v199, s5 op_sel:[0,0,0,1]
	v_cvt_scalef32_pk_fp8_f32 v153, v208, v212, s5 op_sel:[0,0,0,1]
	v_cvt_scalef32_pk_fp8_f32 v157, v209, v213, s5 op_sel:[0,0,0,1]
	v_cvt_scalef32_pk_fp8_f32 v161, v210, v214, s5 op_sel:[0,0,0,1]
	v_cvt_scalef32_pk_fp8_f32 v165, v211, v215, s5 op_sel:[0,0,0,1]
	v_cvt_scalef32_pk_fp8_f32 v154, v224, v228, s5 op_sel:[0,0,0,1]
	v_cvt_scalef32_pk_fp8_f32 v158, v225, v229, s5 op_sel:[0,0,0,1]
	v_cvt_scalef32_pk_fp8_f32 v162, v226, v230, s5 op_sel:[0,0,0,1]
	v_cvt_scalef32_pk_fp8_f32 v166, v227, v231, s5 op_sel:[0,0,0,1]
	v_cvt_scalef32_pk_fp8_f32 v155, v240, v244, s5 op_sel:[0,0,0,1]
	v_cvt_scalef32_pk_fp8_f32 v159, v241, v245, s5 op_sel:[0,0,0,1]
	v_cvt_scalef32_pk_fp8_f32 v163, v242, v246, s5 op_sel:[0,0,0,1]
	v_cvt_scalef32_pk_fp8_f32 v167, v243, v247, s5 op_sel:[0,0,0,1]
	s_add_u32 s100, s100, s88
	s_addc_u32 s101, s101, 0
	global_load_dwordx4 v[184:187], v132, s[100:101] nt
	global_load_dwordx4 v[188:191], v133, s[100:101] nt
	global_load_dwordx4 v[192:195], v134, s[100:101] nt
	global_load_dwordx4 v[196:199], v135, s[100:101] nt
	global_load_dwordx4 v[200:203], v136, s[100:101] nt
	global_load_dwordx4 v[204:207], v137, s[100:101] nt
	global_load_dwordx4 v[208:211], v138, s[100:101] nt
	global_load_dwordx4 v[212:215], v139, s[100:101] nt
	global_load_dwordx4 v[216:219], v140, s[100:101] nt
	global_load_dwordx4 v[220:223], v141, s[100:101] nt
	global_load_dwordx4 v[224:227], v142, s[100:101] nt
	global_load_dwordx4 v[228:231], v143, s[100:101] nt
	global_load_dwordx4 v[232:235], v144, s[100:101] nt
	global_load_dwordx4 v[236:239], v145, s[100:101] nt
	global_load_dwordx4 v[240:243], v146, s[100:101] nt
	global_load_dwordx4 v[244:247], v147, s[100:101] nt
	ds_write_b128 v148, v[152:155] offset:0
	ds_write_b128 v148, v[156:159] offset:128
	ds_write_b128 v149, v[160:163] offset:0
	ds_write_b128 v149, v[164:167] offset:128
	s_waitcnt lgkmcnt(0)
	s_barrier
	ds_read_b128 v[168:171], v150 offset:0
	ds_read_b128 v[172:175], v150 offset:1024
	ds_read_b128 v[176:179], v150 offset:2048
	ds_read_b128 v[180:183], v150 offset:3072
	s_waitcnt lgkmcnt(3)
	global_store_dwordx4 v150, v[168:171], s[6:7] sc1
	s_waitcnt lgkmcnt(2)
	global_store_dwordx4 v150, v[172:175], s[6:7] offset:1024 sc1
	s_waitcnt lgkmcnt(1)
	global_store_dwordx4 v150, v[176:179], s[6:7] offset:2048 sc1
	s_waitcnt lgkmcnt(0)
	global_store_dwordx4 v150, v[180:183], s[6:7] offset:3072 sc1
	s_add_u32 s6, s6, 0x8000
	s_addc_u32 s7, s7, 0
	s_waitcnt vmcnt(44)
	v_cvt_scalef32_pk_fp8_f32 v152, v0, v4, s5
	v_cvt_scalef32_pk_fp8_f32 v156, v1, v5, s5
	v_cvt_scalef32_pk_fp8_f32 v160, v2, v6, s5
	v_cvt_scalef32_pk_fp8_f32 v164, v3, v7, s5
	v_cvt_scalef32_pk_fp8_f32 v153, v16, v20, s5
	v_cvt_scalef32_pk_fp8_f32 v157, v17, v21, s5
	v_cvt_scalef32_pk_fp8_f32 v161, v18, v22, s5
	v_cvt_scalef32_pk_fp8_f32 v165, v19, v23, s5
	v_cvt_scalef32_pk_fp8_f32 v154, v32, v36, s5
	v_cvt_scalef32_pk_fp8_f32 v158, v33, v37, s5
	v_cvt_scalef32_pk_fp8_f32 v162, v34, v38, s5
	v_cvt_scalef32_pk_fp8_f32 v166, v35, v39, s5
	v_cvt_scalef32_pk_fp8_f32 v155, v48, v52, s5
	v_cvt_scalef32_pk_fp8_f32 v159, v49, v53, s5
	v_cvt_scalef32_pk_fp8_f32 v163, v50, v54, s5
	v_cvt_scalef32_pk_fp8_f32 v167, v51, v55, s5
	v_cvt_scalef32_pk_fp8_f32 v152, v8, v12, s5 op_sel:[0,0,0,1]
	v_cvt_scalef32_pk_fp8_f32 v156, v9, v13, s5 op_sel:[0,0,0,1]
	v_cvt_scalef32_pk_fp8_f32 v160, v10, v14, s5 op_sel:[0,0,0,1]
	v_cvt_scalef32_pk_fp8_f32 v164, v11, v15, s5 op_sel:[0,0,0,1]
	v_cvt_scalef32_pk_fp8_f32 v153, v24, v28, s5 op_sel:[0,0,0,1]
	v_cvt_scalef32_pk_fp8_f32 v157, v25, v29, s5 op_sel:[0,0,0,1]
	v_cvt_scalef32_pk_fp8_f32 v161, v26, v30, s5 op_sel:[0,0,0,1]
	v_cvt_scalef32_pk_fp8_f32 v165, v27, v31, s5 op_sel:[0,0,0,1]
	v_cvt_scalef32_pk_fp8_f32 v154, v40, v44, s5 op_sel:[0,0,0,1]
	v_cvt_scalef32_pk_fp8_f32 v158, v41, v45, s5 op_sel:[0,0,0,1]
	v_cvt_scalef32_pk_fp8_f32 v162, v42, v46, s5 op_sel:[0,0,0,1]
	v_cvt_scalef32_pk_fp8_f32 v166, v43, v47, s5 op_sel:[0,0,0,1]
	v_cvt_scalef32_pk_fp8_f32 v155, v56, v60, s5 op_sel:[0,0,0,1]
	v_cvt_scalef32_pk_fp8_f32 v159, v57, v61, s5 op_sel:[0,0,0,1]
	v_cvt_scalef32_pk_fp8_f32 v163, v58, v62, s5 op_sel:[0,0,0,1]
	v_cvt_scalef32_pk_fp8_f32 v167, v59, v63, s5 op_sel:[0,0,0,1]
	s_add_u32 s100, s100, s88
	s_addc_u32 s101, s101, 0
	global_load_dwordx4 v[0:3], v132, s[100:101] nt
	global_load_dwordx4 v[4:7], v133, s[100:101] nt
	global_load_dwordx4 v[8:11], v134, s[100:101] nt
	global_load_dwordx4 v[12:15], v135, s[100:101] nt
	global_load_dwordx4 v[16:19], v136, s[100:101] nt
	global_load_dwordx4 v[20:23], v137, s[100:101] nt
	global_load_dwordx4 v[24:27], v138, s[100:101] nt
	global_load_dwordx4 v[28:31], v139, s[100:101] nt
	global_load_dwordx4 v[32:35], v140, s[100:101] nt
	global_load_dwordx4 v[36:39], v141, s[100:101] nt
	global_load_dwordx4 v[40:43], v142, s[100:101] nt
	global_load_dwordx4 v[44:47], v143, s[100:101] nt
	global_load_dwordx4 v[48:51], v144, s[100:101] nt
	global_load_dwordx4 v[52:55], v145, s[100:101] nt
	global_load_dwordx4 v[56:59], v146, s[100:101] nt
	global_load_dwordx4 v[60:63], v147, s[100:101] nt
	ds_write_b128 v148, v[152:155] offset:32768
	ds_write_b128 v148, v[156:159] offset:32896
	ds_write_b128 v149, v[160:163] offset:32768
	ds_write_b128 v149, v[164:167] offset:32896
	s_waitcnt lgkmcnt(0)
	s_barrier
; #define G_SCHED __builtin_amdgcn_sched_barrier(0)
; #define CI_LOAD(R, kt) do { _Pragma("unroll") for (int _j = 0; _j < 16; ++_j) R[_j] = __builtin_nontemporal_load((const f32x4*)(src + (size_t)((kt) * 128 + _j) * LDB)); } while (0)
; template <int LDB>
; __device__ __forceinline__ void convert_image(const float* __restrict__ W, int col0, int col1, unsigned char* __restrict__ img, LAS3 char* lds, int wid) {
;     ...
;     f32x4 ra[16], rb[16];
;     CI_LOAD(ra, 0);
;     for (int kt = 0; kt < 16; kt += 2) {
;         CI_LOAD(rb, kt + 1); G_SCHED;
;         CI_CONV(ra, kt); G_SCHED;
;         CI_LOAD(ra, (kt + 2 < 16) ? kt + 2 : 15); G_SCHED;
;         CI_CONV(rb, kt + 1); G_SCHED;
;     }
	ds_read_b128 v[168:171], v150 offset:32768
	ds_read_b128 v[172:175], v150 offset:33792
	ds_read_b128 v[176:179], v150 offset:34816
	ds_read_b128 v[180:183], v150 offset:35840
	s_waitcnt lgkmcnt(3)
	global_store_dwordx4 v150, v[168:171], s[6:7] sc1
	s_waitcnt lgkmcnt(2)
	global_store_dwordx4 v150, v[172:175], s[6:7] offset:1024 sc1
	s_waitcnt lgkmcnt(1)
	global_store_dwordx4 v150, v[176:179], s[6:7] offset:2048 sc1
	s_waitcnt lgkmcnt(0)
	global_store_dwordx4 v150, v[180:183], s[6:7] offset:3072 sc1
	s_add_u32 s6, s6, 0x8000
	s_addc_u32 s7, s7, 0
	s_waitcnt vmcnt(44)
	v_cvt_scalef32_pk_fp8_f32 v152, v64, v68, s5
	v_cvt_scalef32_pk_fp8_f32 v156, v65, v69, s5
	v_cvt_scalef32_pk_fp8_f32 v160, v66, v70, s5
	v_cvt_scalef32_pk_fp8_f32 v164, v67, v71, s5
	v_cvt_scalef32_pk_fp8_f32 v153, v80, v84, s5
	v_cvt_scalef32_pk_fp8_f32 v157, v81, v85, s5
	v_cvt_scalef32_pk_fp8_f32 v161, v82, v86, s5
	v_cvt_scalef32_pk_fp8_f32 v165, v83, v87, s5
	v_cvt_scalef32_pk_fp8_f32 v154, v96, v100, s5
	v_cvt_scalef32_pk_fp8_f32 v158, v97, v101, s5
	v_cvt_scalef32_pk_fp8_f32 v162, v98, v102, s5
	v_cvt_scalef32_pk_fp8_f32 v166, v99, v103, s5
	v_cvt_scalef32_pk_fp8_f32 v155, v112, v116, s5
	v_cvt_scalef32_pk_fp8_f32 v159, v113, v117, s5
	v_cvt_scalef32_pk_fp8_f32 v163, v114, v118, s5
	v_cvt_scalef32_pk_fp8_f32 v167, v115, v119, s5
	v_cvt_scalef32_pk_fp8_f32 v152, v72, v76, s5 op_sel:[0,0,0,1]
	v_cvt_scalef32_pk_fp8_f32 v156, v73, v77, s5 op_sel:[0,0,0,1]
	v_cvt_scalef32_pk_fp8_f32 v160, v74, v78, s5 op_sel:[0,0,0,1]
	v_cvt_scalef32_pk_fp8_f32 v164, v75, v79, s5 op_sel:[0,0,0,1]
	v_cvt_scalef32_pk_fp8_f32 v153, v88, v92, s5 op_sel:[0,0,0,1]
	v_cvt_scalef32_pk_fp8_f32 v157, v89, v93, s5 op_sel:[0,0,0,1]
	v_cvt_scalef32_pk_fp8_f32 v161, v90, v94, s5 op_sel:[0,0,0,1]
	v_cvt_scalef32_pk_fp8_f32 v165, v91, v95, s5 op_sel:[0,0,0,1]
	v_cvt_scalef32_pk_fp8_f32 v154, v104, v108, s5 op_sel:[0,0,0,1]
	v_cvt_scalef32_pk_fp8_f32 v158, v105, v109, s5 op_sel:[0,0,0,1]
	v_cvt_scalef32_pk_fp8_f32 v162, v106, v110, s5 op_sel:[0,0,0,1]
	v_cvt_scalef32_pk_fp8_f32 v166, v107, v111, s5 op_sel:[0,0,0,1]
	v_cvt_scalef32_pk_fp8_f32 v155, v120, v124, s5 op_sel:[0,0,0,1]
	v_cvt_scalef32_pk_fp8_f32 v159, v121, v125, s5 op_sel:[0,0,0,1]
	v_cvt_scalef32_pk_fp8_f32 v163, v122, v126, s5 op_sel:[0,0,0,1]
	v_cvt_scalef32_pk_fp8_f32 v167, v123, v127, s5 op_sel:[0,0,0,1]
	s_add_u32 s100, s100, s88
	s_addc_u32 s101, s101, 0
	global_load_dwordx4 v[64:67], v132, s[100:101] nt
	global_load_dwordx4 v[68:71], v133, s[100:101] nt
	global_load_dwordx4 v[72:75], v134, s[100:101] nt
	global_load_dwordx4 v[76:79], v135, s[100:101] nt
	global_load_dwordx4 v[80:83], v136, s[100:101] nt
	global_load_dwordx4 v[84:87], v137, s[100:101] nt
	global_load_dwordx4 v[88:91], v138, s[100:101] nt
	global_load_dwordx4 v[92:95], v139, s[100:101] nt
	global_load_dwordx4 v[96:99], v140, s[100:101] nt
	global_load_dwordx4 v[100:103], v141, s[100:101] nt
	global_load_dwordx4 v[104:107], v142, s[100:101] nt
	global_load_dwordx4 v[108:111], v143, s[100:101] nt
	global_load_dwordx4 v[112:115], v144, s[100:101] nt
	global_load_dwordx4 v[116:119], v145, s[100:101] nt
	global_load_dwordx4 v[120:123], v146, s[100:101] nt
	global_load_dwordx4 v[124:127], v147, s[100:101] nt
	ds_write_b128 v148, v[152:155] offset:0
	ds_write_b128 v148, v[156:159] offset:128
	ds_write_b128 v149, v[160:163] offset:0
	ds_write_b128 v149, v[164:167] offset:128
	s_waitcnt lgkmcnt(0)
	s_barrier
	ds_read_b128 v[168:171], v150 offset:0
	ds_read_b128 v[172:175], v150 offset:1024
	ds_read_b128 v[176:179], v150 offset:2048
	ds_read_b128 v[180:183], v150 offset:3072
	s_waitcnt lgkmcnt(3)
	global_store_dwordx4 v150, v[168:171], s[6:7] sc1
	s_waitcnt lgkmcnt(2)
	global_store_dwordx4 v150, v[172:175], s[6:7] offset:1024 sc1
	s_waitcnt lgkmcnt(1)
	global_store_dwordx4 v150, v[176:179], s[6:7] offset:2048 sc1
	s_waitcnt lgkmcnt(0)
	global_store_dwordx4 v150, v[180:183], s[6:7] offset:3072 sc1
	s_add_u32 s6, s6, 0x8000
	s_addc_u32 s7, s7, 0
	s_waitcnt vmcnt(44)
	v_cvt_scalef32_pk_fp8_f32 v152, v184, v188, s5
	v_cvt_scalef32_pk_fp8_f32 v156, v185, v189, s5
	v_cvt_scalef32_pk_fp8_f32 v160, v186, v190, s5
	v_cvt_scalef32_pk_fp8_f32 v164, v187, v191, s5
	v_cvt_scalef32_pk_fp8_f32 v153, v200, v204, s5
	v_cvt_scalef32_pk_fp8_f32 v157, v201, v205, s5
	v_cvt_scalef32_pk_fp8_f32 v161, v202, v206, s5
	v_cvt_scalef32_pk_fp8_f32 v165, v203, v207, s5
	v_cvt_scalef32_pk_fp8_f32 v154, v216, v220, s5
	v_cvt_scalef32_pk_fp8_f32 v158, v217, v221, s5
	v_cvt_scalef32_pk_fp8_f32 v162, v218, v222, s5
	v_cvt_scalef32_pk_fp8_f32 v166, v219, v223, s5
	v_cvt_scalef32_pk_fp8_f32 v155, v232, v236, s5
	v_cvt_scalef32_pk_fp8_f32 v159, v233, v237, s5
	v_cvt_scalef32_pk_fp8_f32 v163, v234, v238, s5
	v_cvt_scalef32_pk_fp8_f32 v167, v235, v239, s5
	v_cvt_scalef32_pk_fp8_f32 v152, v192, v196, s5 op_sel:[0,0,0,1]
	v_cvt_scalef32_pk_fp8_f32 v156, v193, v197, s5 op_sel:[0,0,0,1]
	v_cvt_scalef32_pk_fp8_f32 v160, v194, v198, s5 op_sel:[0,0,0,1]
	v_cvt_scalef32_pk_fp8_f32 v164, v195, v199, s5 op_sel:[0,0,0,1]
	v_cvt_scalef32_pk_fp8_f32 v153, v208, v212, s5 op_sel:[0,0,0,1]
	v_cvt_scalef32_pk_fp8_f32 v157, v209, v213, s5 op_sel:[0,0,0,1]
	v_cvt_scalef32_pk_fp8_f32 v161, v210, v214, s5 op_sel:[0,0,0,1]
	v_cvt_scalef32_pk_fp8_f32 v165, v211, v215, s5 op_sel:[0,0,0,1]
	v_cvt_scalef32_pk_fp8_f32 v154, v224, v228, s5 op_sel:[0,0,0,1]
	v_cvt_scalef32_pk_fp8_f32 v158, v225, v229, s5 op_sel:[0,0,0,1]
	v_cvt_scalef32_pk_fp8_f32 v162, v226, v230, s5 op_sel:[0,0,0,1]
	v_cvt_scalef32_pk_fp8_f32 v166, v227, v231, s5 op_sel:[0,0,0,1]
	v_cvt_scalef32_pk_fp8_f32 v155, v240, v244, s5 op_sel:[0,0,0,1]
	v_cvt_scalef32_pk_fp8_f32 v159, v241, v245, s5 op_sel:[0,0,0,1]
	v_cvt_scalef32_pk_fp8_f32 v163, v242, v246, s5 op_sel:[0,0,0,1]
	v_cvt_scalef32_pk_fp8_f32 v167, v243, v247, s5 op_sel:[0,0,0,1]
	s_add_u32 s100, s100, s88
	s_addc_u32 s101, s101, 0
	global_load_dwordx4 v[184:187], v132, s[100:101] nt
	global_load_dwordx4 v[188:191], v133, s[100:101] nt
	global_load_dwordx4 v[192:195], v134, s[100:101] nt
	global_load_dwordx4 v[196:199], v135, s[100:101] nt
	global_load_dwordx4 v[200:203], v136, s[100:101] nt
	global_load_dwordx4 v[204:207], v137, s[100:101] nt
	global_load_dwordx4 v[208:211], v138, s[100:101] nt
	global_load_dwordx4 v[212:215], v139, s[100:101] nt
	global_load_dwordx4 v[216:219], v140, s[100:101] nt
	global_load_dwordx4 v[220:223], v141, s[100:101] nt
	global_load_dwordx4 v[224:227], v142, s[100:101] nt
	global_load_dwordx4 v[228:231], v143, s[100:101] nt
	global_load_dwordx4 v[232:235], v144, s[100:101] nt
	global_load_dwordx4 v[236:239], v145, s[100:101] nt
	global_load_dwordx4 v[240:243], v146, s[100:101] nt
	global_load_dwordx4 v[244:247], v147, s[100:101] nt
	ds_write_b128 v148, v[152:155] offset:32768
	ds_write_b128 v148, v[156:159] offset:32896
	ds_write_b128 v149, v[160:163] offset:32768
	ds_write_b128 v149, v[164:167] offset:32896
	s_waitcnt lgkmcnt(0)
	s_barrier
; #define G_SCHED __builtin_amdgcn_sched_barrier(0)
; #define CI_LOAD(R, kt) do { _Pragma("unroll") for (int _j = 0; _j < 16; ++_j) R[_j] = __builtin_nontemporal_load((const f32x4*)(src + (size_t)((kt) * 128 + _j) * LDB)); } while (0)
; template <int LDB>
; __device__ __forceinline__ void convert_image(const float* __restrict__ W, int col0, int col1, unsigned char* __restrict__ img, LAS3 char* lds, int wid) {
;     ...
;     f32x4 ra[16], rb[16];
;     CI_LOAD(ra, 0);
;     for (int kt = 0; kt < 16; kt += 2) {
;         CI_LOAD(rb, kt + 1); G_SCHED;
;         CI_CONV(ra, kt); G_SCHED;
;         CI_LOAD(ra, (kt + 2 < 16) ? kt + 2 : 15); G_SCHED;
;         CI_CONV(rb, kt + 1); G_SCHED;
;     }
	ds_read_b128 v[168:171], v150 offset:32768
	ds_read_b128 v[172:175], v150 offset:33792
	ds_read_b128 v[176:179], v150 offset:34816
	ds_read_b128 v[180:183], v150 offset:35840
	s_waitcnt lgkmcnt(3)
	global_store_dwordx4 v150, v[168:171], s[6:7] sc1
	s_waitcnt lgkmcnt(2)
	global_store_dwordx4 v150, v[172:175], s[6:7] offset:1024 sc1
	s_waitcnt lgkmcnt(1)
	global_store_dwordx4 v150, v[176:179], s[6:7] offset:2048 sc1
	s_waitcnt lgkmcnt(0)
	global_store_dwordx4 v150, v[180:183], s[6:7] offset:3072 sc1
	s_add_u32 s6, s6, 0x8000
	s_addc_u32 s7, s7, 0
	s_waitcnt vmcnt(44)
	v_cvt_scalef32_pk_fp8_f32 v152, v0, v4, s5
	v_cvt_scalef32_pk_fp8_f32 v156, v1, v5, s5
	v_cvt_scalef32_pk_fp8_f32 v160, v2, v6, s5
	v_cvt_scalef32_pk_fp8_f32 v164, v3, v7, s5
	v_cvt_scalef32_pk_fp8_f32 v153, v16, v20, s5
	v_cvt_scalef32_pk_fp8_f32 v157, v17, v21, s5
	v_cvt_scalef32_pk_fp8_f32 v161, v18, v22, s5
	v_cvt_scalef32_pk_fp8_f32 v165, v19, v23, s5
	v_cvt_scalef32_pk_fp8_f32 v154, v32, v36, s5
	v_cvt_scalef32_pk_fp8_f32 v158, v33, v37, s5
	v_cvt_scalef32_pk_fp8_f32 v162, v34, v38, s5
	v_cvt_scalef32_pk_fp8_f32 v166, v35, v39, s5
	v_cvt_scalef32_pk_fp8_f32 v155, v48, v52, s5
	v_cvt_scalef32_pk_fp8_f32 v159, v49, v53, s5
	v_cvt_scalef32_pk_fp8_f32 v163, v50, v54, s5
	v_cvt_scalef32_pk_fp8_f32 v167, v51, v55, s5
	v_cvt_scalef32_pk_fp8_f32 v152, v8, v12, s5 op_sel:[0,0,0,1]
	v_cvt_scalef32_pk_fp8_f32 v156, v9, v13, s5 op_sel:[0,0,0,1]
	v_cvt_scalef32_pk_fp8_f32 v160, v10, v14, s5 op_sel:[0,0,0,1]
	v_cvt_scalef32_pk_fp8_f32 v164, v11, v15, s5 op_sel:[0,0,0,1]
	v_cvt_scalef32_pk_fp8_f32 v153, v24, v28, s5 op_sel:[0,0,0,1]
	v_cvt_scalef32_pk_fp8_f32 v157, v25, v29, s5 op_sel:[0,0,0,1]
	v_cvt_scalef32_pk_fp8_f32 v161, v26, v30, s5 op_sel:[0,0,0,1]
	v_cvt_scalef32_pk_fp8_f32 v165, v27, v31, s5 op_sel:[0,0,0,1]
	v_cvt_scalef32_pk_fp8_f32 v154, v40, v44, s5 op_sel:[0,0,0,1]
	v_cvt_scalef32_pk_fp8_f32 v158, v41, v45, s5 op_sel:[0,0,0,1]
	v_cvt_scalef32_pk_fp8_f32 v162, v42, v46, s5 op_sel:[0,0,0,1]
	v_cvt_scalef32_pk_fp8_f32 v166, v43, v47, s5 op_sel:[0,0,0,1]
	v_cvt_scalef32_pk_fp8_f32 v155, v56, v60, s5 op_sel:[0,0,0,1]
	v_cvt_scalef32_pk_fp8_f32 v159, v57, v61, s5 op_sel:[0,0,0,1]
	v_cvt_scalef32_pk_fp8_f32 v163, v58, v62, s5 op_sel:[0,0,0,1]
	v_cvt_scalef32_pk_fp8_f32 v167, v59, v63, s5 op_sel:[0,0,0,1]
	s_add_u32 s100, s100, s88
	s_addc_u32 s101, s101, 0
	global_load_dwordx4 v[0:3], v132, s[100:101] nt
	global_load_dwordx4 v[4:7], v133, s[100:101] nt
	global_load_dwordx4 v[8:11], v134, s[100:101] nt
	global_load_dwordx4 v[12:15], v135, s[100:101] nt
	global_load_dwordx4 v[16:19], v136, s[100:101] nt
	global_load_dwordx4 v[20:23], v137, s[100:101] nt
	global_load_dwordx4 v[24:27], v138, s[100:101] nt
	global_load_dwordx4 v[28:31], v139, s[100:101] nt
	global_load_dwordx4 v[32:35], v140, s[100:101] nt
	global_load_dwordx4 v[36:39], v141, s[100:101] nt
	global_load_dwordx4 v[40:43], v142, s[100:101] nt
	global_load_dwordx4 v[44:47], v143, s[100:101] nt
	global_load_dwordx4 v[48:51], v144, s[100:101] nt
	global_load_dwordx4 v[52:55], v145, s[100:101] nt
	global_load_dwordx4 v[56:59], v146, s[100:101] nt
	global_load_dwordx4 v[60:63], v147, s[100:101] nt
	ds_write_b128 v148, v[152:155] offset:0
	ds_write_b128 v148, v[156:159] offset:128
	ds_write_b128 v149, v[160:163] offset:0
	ds_write_b128 v149, v[164:167] offset:128
	s_waitcnt lgkmcnt(0)
	s_barrier
	ds_read_b128 v[168:171], v150 offset:0
	ds_read_b128 v[172:175], v150 offset:1024
	ds_read_b128 v[176:179], v150 offset:2048
	ds_read_b128 v[180:183], v150 offset:3072
	s_waitcnt lgkmcnt(3)
	global_store_dwordx4 v150, v[168:171], s[6:7] sc1
	s_waitcnt lgkmcnt(2)
	global_store_dwordx4 v150, v[172:175], s[6:7] offset:1024 sc1
	s_waitcnt lgkmcnt(1)
	global_store_dwordx4 v150, v[176:179], s[6:7] offset:2048 sc1
	s_waitcnt lgkmcnt(0)
	global_store_dwordx4 v150, v[180:183], s[6:7] offset:3072 sc1
	s_add_u32 s6, s6, 0x8000
	s_addc_u32 s7, s7, 0
	s_waitcnt vmcnt(44)
	v_cvt_scalef32_pk_fp8_f32 v152, v64, v68, s5
	v_cvt_scalef32_pk_fp8_f32 v156, v65, v69, s5
	v_cvt_scalef32_pk_fp8_f32 v160, v66, v70, s5
	v_cvt_scalef32_pk_fp8_f32 v164, v67, v71, s5
	v_cvt_scalef32_pk_fp8_f32 v153, v80, v84, s5
	v_cvt_scalef32_pk_fp8_f32 v157, v81, v85, s5
	v_cvt_scalef32_pk_fp8_f32 v161, v82, v86, s5
	v_cvt_scalef32_pk_fp8_f32 v165, v83, v87, s5
	v_cvt_scalef32_pk_fp8_f32 v154, v96, v100, s5
	v_cvt_scalef32_pk_fp8_f32 v158, v97, v101, s5
	v_cvt_scalef32_pk_fp8_f32 v162, v98, v102, s5
	v_cvt_scalef32_pk_fp8_f32 v166, v99, v103, s5
	v_cvt_scalef32_pk_fp8_f32 v155, v112, v116, s5
	v_cvt_scalef32_pk_fp8_f32 v159, v113, v117, s5
	v_cvt_scalef32_pk_fp8_f32 v163, v114, v118, s5
	v_cvt_scalef32_pk_fp8_f32 v167, v115, v119, s5
	v_cvt_scalef32_pk_fp8_f32 v152, v72, v76, s5 op_sel:[0,0,0,1]
	v_cvt_scalef32_pk_fp8_f32 v156, v73, v77, s5 op_sel:[0,0,0,1]
	v_cvt_scalef32_pk_fp8_f32 v160, v74, v78, s5 op_sel:[0,0,0,1]
	v_cvt_scalef32_pk_fp8_f32 v164, v75, v79, s5 op_sel:[0,0,0,1]
	v_cvt_scalef32_pk_fp8_f32 v153, v88, v92, s5 op_sel:[0,0,0,1]
	v_cvt_scalef32_pk_fp8_f32 v157, v89, v93, s5 op_sel:[0,0,0,1]
	v_cvt_scalef32_pk_fp8_f32 v161, v90, v94, s5 op_sel:[0,0,0,1]
	v_cvt_scalef32_pk_fp8_f32 v165, v91, v95, s5 op_sel:[0,0,0,1]
	v_cvt_scalef32_pk_fp8_f32 v154, v104, v108, s5 op_sel:[0,0,0,1]
	v_cvt_scalef32_pk_fp8_f32 v158, v105, v109, s5 op_sel:[0,0,0,1]
	v_cvt_scalef32_pk_fp8_f32 v162, v106, v110, s5 op_sel:[0,0,0,1]
	v_cvt_scalef32_pk_fp8_f32 v166, v107, v111, s5 op_sel:[0,0,0,1]
	v_cvt_scalef32_pk_fp8_f32 v155, v120, v124, s5 op_sel:[0,0,0,1]
	v_cvt_scalef32_pk_fp8_f32 v159, v121, v125, s5 op_sel:[0,0,0,1]
	v_cvt_scalef32_pk_fp8_f32 v163, v122, v126, s5 op_sel:[0,0,0,1]
	v_cvt_scalef32_pk_fp8_f32 v167, v123, v127, s5 op_sel:[0,0,0,1]
	ds_write_b128 v148, v[152:155] offset:32768
	ds_write_b128 v148, v[156:159] offset:32896
	ds_write_b128 v149, v[160:163] offset:32768
	ds_write_b128 v149, v[164:167] offset:32896
	s_waitcnt lgkmcnt(0)
	s_barrier
; #define G_SCHED __builtin_amdgcn_sched_barrier(0)
; #define CI_LOAD(R, kt) do { _Pragma("unroll") for (int _j = 0; _j < 16; ++_j) R[_j] = __builtin_nontemporal_load((const f32x4*)(src + (size_t)((kt) * 128 + _j) * LDB)); } while (0)
; template <int LDB>
; __device__ __forceinline__ void convert_image(const float* __restrict__ W, int col0, int col1, unsigned char* __restrict__ img, LAS3 char* lds, int wid) {
;     ...
;     f32x4 ra[16], rb[16];
;     CI_LOAD(ra, 0);
;     for (int kt = 0; kt < 16; kt += 2) {
;         CI_LOAD(rb, kt + 1); G_SCHED;
;         CI_CONV(ra, kt); G_SCHED;
;         CI_LOAD(ra, (kt + 2 < 16) ? kt + 2 : 15); G_SCHED;
;         CI_CONV(rb, kt + 1); G_SCHED;
;     }
;     asm volatile("s_waitcnt vmcnt(0)" ::: "memory");
;     __syncthreads();
	ds_read_b128 v[168:171], v150 offset:32768
	ds_read_b128 v[172:175], v150 offset:33792
	ds_read_b128 v[176:179], v150 offset:34816
	ds_read_b128 v[180:183], v150 offset:35840
	s_waitcnt lgkmcnt(3)
	global_store_dwordx4 v150, v[168:171], s[6:7] sc1
	s_waitcnt lgkmcnt(2)
	global_store_dwordx4 v150, v[172:175], s[6:7] offset:1024 sc1
	s_waitcnt lgkmcnt(1)
	global_store_dwordx4 v150, v[176:179], s[6:7] offset:2048 sc1
	s_waitcnt lgkmcnt(0)
	global_store_dwordx4 v150, v[180:183], s[6:7] offset:3072 sc1
	s_add_u32 s6, s6, 0x8000
	s_addc_u32 s7, s7, 0
	s_waitcnt vmcnt(28)
	v_cvt_scalef32_pk_fp8_f32 v152, v184, v188, s5
	v_cvt_scalef32_pk_fp8_f32 v156, v185, v189, s5
	v_cvt_scalef32_pk_fp8_f32 v160, v186, v190, s5
	v_cvt_scalef32_pk_fp8_f32 v164, v187, v191, s5
	v_cvt_scalef32_pk_fp8_f32 v153, v200, v204, s5
	v_cvt_scalef32_pk_fp8_f32 v157, v201, v205, s5
	v_cvt_scalef32_pk_fp8_f32 v161, v202, v206, s5
	v_cvt_scalef32_pk_fp8_f32 v165, v203, v207, s5
	v_cvt_scalef32_pk_fp8_f32 v154, v216, v220, s5
	v_cvt_scalef32_pk_fp8_f32 v158, v217, v221, s5
	v_cvt_scalef32_pk_fp8_f32 v162, v218, v222, s5
	v_cvt_scalef32_pk_fp8_f32 v166, v219, v223, s5
	v_cvt_scalef32_pk_fp8_f32 v155, v232, v236, s5
	v_cvt_scalef32_pk_fp8_f32 v159, v233, v237, s5
	v_cvt_scalef32_pk_fp8_f32 v163, v234, v238, s5
	v_cvt_scalef32_pk_fp8_f32 v167, v235, v239, s5
	v_cvt_scalef32_pk_fp8_f32 v152, v192, v196, s5 op_sel:[0,0,0,1]
	v_cvt_scalef32_pk_fp8_f32 v156, v193, v197, s5 op_sel:[0,0,0,1]
	v_cvt_scalef32_pk_fp8_f32 v160, v194, v198, s5 op_sel:[0,0,0,1]
	v_cvt_scalef32_pk_fp8_f32 v164, v195, v199, s5 op_sel:[0,0,0,1]
	v_cvt_scalef32_pk_fp8_f32 v153, v208, v212, s5 op_sel:[0,0,0,1]
	v_cvt_scalef32_pk_fp8_f32 v157, v209, v213, s5 op_sel:[0,0,0,1]
	v_cvt_scalef32_pk_fp8_f32 v161, v210, v214, s5 op_sel:[0,0,0,1]
	v_cvt_scalef32_pk_fp8_f32 v165, v211, v215, s5 op_sel:[0,0,0,1]
	v_cvt_scalef32_pk_fp8_f32 v154, v224, v228, s5 op_sel:[0,0,0,1]
	v_cvt_scalef32_pk_fp8_f32 v158, v225, v229, s5 op_sel:[0,0,0,1]
	v_cvt_scalef32_pk_fp8_f32 v162, v226, v230, s5 op_sel:[0,0,0,1]
	v_cvt_scalef32_pk_fp8_f32 v166, v227, v231, s5 op_sel:[0,0,0,1]
	v_cvt_scalef32_pk_fp8_f32 v155, v240, v244, s5 op_sel:[0,0,0,1]
	v_cvt_scalef32_pk_fp8_f32 v159, v241, v245, s5 op_sel:[0,0,0,1]
	v_cvt_scalef32_pk_fp8_f32 v163, v242, v246, s5 op_sel:[0,0,0,1]
	v_cvt_scalef32_pk_fp8_f32 v167, v243, v247, s5 op_sel:[0,0,0,1]
	ds_write_b128 v148, v[152:155] offset:0
	ds_write_b128 v148, v[156:159] offset:128
	ds_write_b128 v149, v[160:163] offset:0
	ds_write_b128 v149, v[164:167] offset:128
	s_waitcnt lgkmcnt(0)
	s_barrier
	ds_read_b128 v[168:171], v150 offset:0
	ds_read_b128 v[172:175], v150 offset:1024
	ds_read_b128 v[176:179], v150 offset:2048
	ds_read_b128 v[180:183], v150 offset:3072
	s_waitcnt lgkmcnt(3)
	global_store_dwordx4 v150, v[168:171], s[6:7] sc1
	s_waitcnt lgkmcnt(2)
	global_store_dwordx4 v150, v[172:175], s[6:7] offset:1024 sc1
	s_waitcnt lgkmcnt(1)
	global_store_dwordx4 v150, v[176:179], s[6:7] offset:2048 sc1
	s_waitcnt lgkmcnt(0)
	global_store_dwordx4 v150, v[180:183], s[6:7] offset:3072 sc1
	s_add_u32 s6, s6, 0x8000
	s_addc_u32 s7, s7, 0
	s_waitcnt vmcnt(12)
	v_cvt_scalef32_pk_fp8_f32 v152, v0, v4, s5
	v_cvt_scalef32_pk_fp8_f32 v156, v1, v5, s5
	v_cvt_scalef32_pk_fp8_f32 v160, v2, v6, s5
	v_cvt_scalef32_pk_fp8_f32 v164, v3, v7, s5
	v_cvt_scalef32_pk_fp8_f32 v153, v16, v20, s5
	v_cvt_scalef32_pk_fp8_f32 v157, v17, v21, s5
	v_cvt_scalef32_pk_fp8_f32 v161, v18, v22, s5
	v_cvt_scalef32_pk_fp8_f32 v165, v19, v23, s5
	v_cvt_scalef32_pk_fp8_f32 v154, v32, v36, s5
	v_cvt_scalef32_pk_fp8_f32 v158, v33, v37, s5
	v_cvt_scalef32_pk_fp8_f32 v162, v34, v38, s5
	v_cvt_scalef32_pk_fp8_f32 v166, v35, v39, s5
	v_cvt_scalef32_pk_fp8_f32 v155, v48, v52, s5
	v_cvt_scalef32_pk_fp8_f32 v159, v49, v53, s5
	v_cvt_scalef32_pk_fp8_f32 v163, v50, v54, s5
	v_cvt_scalef32_pk_fp8_f32 v167, v51, v55, s5
	v_cvt_scalef32_pk_fp8_f32 v152, v8, v12, s5 op_sel:[0,0,0,1]
	v_cvt_scalef32_pk_fp8_f32 v156, v9, v13, s5 op_sel:[0,0,0,1]
	v_cvt_scalef32_pk_fp8_f32 v160, v10, v14, s5 op_sel:[0,0,0,1]
	v_cvt_scalef32_pk_fp8_f32 v164, v11, v15, s5 op_sel:[0,0,0,1]
	v_cvt_scalef32_pk_fp8_f32 v153, v24, v28, s5 op_sel:[0,0,0,1]
	v_cvt_scalef32_pk_fp8_f32 v157, v25, v29, s5 op_sel:[0,0,0,1]
	v_cvt_scalef32_pk_fp8_f32 v161, v26, v30, s5 op_sel:[0,0,0,1]
	v_cvt_scalef32_pk_fp8_f32 v165, v27, v31, s5 op_sel:[0,0,0,1]
	v_cvt_scalef32_pk_fp8_f32 v154, v40, v44, s5 op_sel:[0,0,0,1]
	v_cvt_scalef32_pk_fp8_f32 v158, v41, v45, s5 op_sel:[0,0,0,1]
	v_cvt_scalef32_pk_fp8_f32 v162, v42, v46, s5 op_sel:[0,0,0,1]
	v_cvt_scalef32_pk_fp8_f32 v166, v43, v47, s5 op_sel:[0,0,0,1]
	v_cvt_scalef32_pk_fp8_f32 v155, v56, v60, s5 op_sel:[0,0,0,1]
	v_cvt_scalef32_pk_fp8_f32 v159, v57, v61, s5 op_sel:[0,0,0,1]
	v_cvt_scalef32_pk_fp8_f32 v163, v58, v62, s5 op_sel:[0,0,0,1]
	v_cvt_scalef32_pk_fp8_f32 v167, v59, v63, s5 op_sel:[0,0,0,1]
	ds_write_b128 v148, v[152:155] offset:32768
	ds_write_b128 v148, v[156:159] offset:32896
	ds_write_b128 v149, v[160:163] offset:32768
	ds_write_b128 v149, v[164:167] offset:32896
	s_waitcnt lgkmcnt(0)
	s_barrier
	ds_read_b128 v[168:171], v150 offset:32768
	ds_read_b128 v[172:175], v150 offset:33792
	ds_read_b128 v[176:179], v150 offset:34816
	ds_read_b128 v[180:183], v150 offset:35840
	s_waitcnt lgkmcnt(3)
	global_store_dwordx4 v150, v[168:171], s[6:7] sc1
	s_waitcnt lgkmcnt(2)
	global_store_dwordx4 v150, v[172:175], s[6:7] offset:1024 sc1
	s_waitcnt lgkmcnt(1)
	global_store_dwordx4 v150, v[176:179], s[6:7] offset:2048 sc1
	s_waitcnt lgkmcnt(0)
	global_store_dwordx4 v150, v[180:183], s[6:7] offset:3072 sc1
	s_add_u32 s6, s6, 0x8000
	s_addc_u32 s7, s7, 0
	s_waitcnt vmcnt(0)
	s_barrier
	s_cmp_lg_u32 vcc_hi, 0
	s_cbranch_scc1 .Lpc_skip
	v_mov_b32_e32 v152, 0
	v_mov_b32_e32 v153, 1
	v_cmp_eq_u32_e32 vcc, 0, v131
	s_and_saveexec_b64 s[4:5], vcc
	global_store_dword v152, v153, s[0:1] sc1
	s_mov_b64 exec, s[4:5]
.Lpc_skip:
	s_cmpk_gt_i32 s87, 0x2ff
	s_cbranch_scc1 .LBB0_116
	s_mov_b64 s[6:7], -1
	s_and_b64 vcc, exec, s[76:77]
	s_cbranch_vccz .LBB0_81
	s_cmpk_gt_i32 s87, 0x1ff
	s_cbranch_scc0 .LBB0_78
	s_add_i32 s0, s87, 0xfffffe00
	s_lshr_b32 s0, s0, 6
	s_add_i32 s4, s0, 16
	s_and_b32 s88, s87, 31
	s_bfe_u32 s0, s87, 0x10005
	s_mov_b64 s[6:7], 0

; template <int EPI>
; __device__ __forceinline__ void gemm_tile_img(const GemmArgs& g, int pm, int pn, int e, int ebase, int ecnt, LAS3 char* lds, int wid, const unsigned char* img, const TileSync& sy, int kh = -1) {
;     ...
;     if (EPI >= 2) { fl0 = ld_early(sy.flag); dp0 = ld_early(sy.dep ? sy.dep : sy.flag); }
;     unsigned aoff[2][2];
; #pragma unroll
;     for (int h = 0; h < 2; ++h)
; #pragma unroll
;         for (int i = 0; i < 2; ++i) {
;             const int rih = (i * 8 + wid) * 8 + (lane >> 3);
;             const int chunk = (lane & 7) ^ ((rih >> 1) & 7);
;             int r = pm * 256 + h * 128 + rih;
;             unsigned grow;
;             if (EPI == 2) { if (r >= ecnt) r = ecnt - 1; grow = (unsigned)(g.list[e * T + r] >> 2); }
;             else if (EPI == 3) { grow = (unsigned)(((g.abase >> 8) + pm) * (16 * 256) + h * 128 + rih); }
;             else grow = (unsigned)r;
;             aoff[h][i] = (EPI == 3) ? (grow * 128u + (unsigned)(chunk * 16)) : (EPI >= 2) ? (grow * (unsigned)D + (unsigned)(chunk * 16)) : (grow * (unsigned)D + (unsigned)(chunk * 8)) * 2u;
;         }
;     if (EPI >= 2) {
;         if (tid < 256) {
;             float bvv;
;             if (EPI == 2) bvv = (tid < 128) ? g.bias[(size_t)e * (2 * DFF) + pn * 128 + tid] : g.bias[(size_t)e * (2 * DFF) + DFF + pn * 128 + (tid - 128)] + 1.0f;
;             else bvv = g.bias[(size_t)e * D + pn * 256 + tid];
;             *(LAS3 float*)(lds + LDS_BIAS + tid * 4) = bvv;
; template <int EPI>
; __device__ __forceinline__ int* moe_phase(const Params& p, LAS3 char* lds, int wid, int* pend_in) {
;     ...
;             } else if (sl >= 0 && sl < NS) {
;                 const int e = qq + 8 * (sl / NCOL), pn = sl % NCOL;
;                 const int ecnt = __builtin_amdgcn_readfirstlane(xcnt[e]), ebase = __builtin_amdgcn_readfirstlane(xcnt[32 + e]), abase = __builtin_amdgcn_readfirstlane(xcnt[64 + e]); g.abase = abase;
;                 if (k < ((ecnt + 255) >> 8)) {
;                     TileSync sy{}; sy.flag = p.flag + ((EPI == 2) ? 0 : NE * 16) + e * NCOL + pn; sy.qctr = qctr + qq; sy.qtag = (unsigned)qq << 20; sy.qslot = slot + (par ^ 1);
;                     if (MOE_MERGED) { sy.pend = pend; if (EPI == 3) { sy.dep = p.done + e * 32 + k; sy.depn = 16; } }
;                     unsigned char* img = ((EPI == 2) ? p.img_gu : p.img_dn) + (size_t)(e * NCOL + pn) * 524288;
.LBB0_450:
	s_sub_i32 s27, s26, s4
	v_cndmask_b32_e64 v2, 0, 1, s[24:25]
	v_cmp_eq_u32_e32 vcc, s27, v2
	s_and_b64 s[14:15], s[0:1], vcc
	s_andn2_b64 vcc, exec, s[14:15]
	s_mov_b64 s[14:15], -1
	s_cbranch_vccz .LBB0_495
	s_cmp_eq_u32 s26, s4
	s_cselect_b64 s[14:15], -1, 0
	s_and_b64 s[24:25], s[24:25], s[14:15]
	s_add_i32 s4, s12, -15
	s_and_b64 s[14:15], s[24:25], exec
	s_cselect_b32 s13, s12, s4
	s_mov_b64 s[14:15], 0
	s_cmp_gt_u32 s13, 63
	v_mov_b64_e32 v[0:1], v[252:253]
	s_mov_b64 s[16:17], 0
	s_cbranch_scc1 .LBB0_495
	v_readfirstlane_b32 s4, v2
	v_cndmask_b32_e64 v0, 0, 1, s[0:1]
	s_sub_i32 s4, s27, s4
	v_readfirstlane_b32 s0, v0
	s_sub_i32 s4, s4, s0
	s_and_b64 s[0:1], s[24:25], exec
	s_cselect_b32 s38, 0, s4
	s_lshr_b32 s0, s13, 1
	s_and_b32 s26, s0, 24
	s_add_i32 s26, s26, s86
	s_lshl_b32 s0, s26, 2
	s_add_i32 s0, s0, 0
	s_add_i32 s0, s0, 0x21400
	v_mov_b32_e32 v0, s0
	ds_read2st64_b32 v[0:1], v0 offset1:1
	s_mov_b32 s36, s38
	s_waitcnt lgkmcnt(0)
	v_readfirstlane_b32 s27, v0
	v_readfirstlane_b32 s0, v1
	v_mov_b64_e32 v[0:1], v[252:253]
	s_nop 0
	v_writelane_b32 v255, s0, 12
	s_add_i32 s0, s27, 0xff
	s_ashr_i32 s0, s0, 8
	v_writelane_b32 v255, s36, 13
	s_cmp_ge_i32 s38, s0
	s_nop 0
	v_writelane_b32 v255, s37, 14
	s_cbranch_scc1 .LBB0_495
	v_readlane_b32 s36, v254, 20
	s_xor_b64 s[0:1], s[24:25], -1
	s_lshl_b32 s24, s86, 1
	s_add_i32 s24, s24, s13
	s_and_b32 s24, s24, 15
	s_lshl_b32 s16, s26, 6
	v_readlane_b32 s46, v254, 30
	v_readlane_b32 s47, v254, 31
	s_add_u32 s16, s46, s16
	s_addc_u32 s17, s47, 0
	s_lshl_b32 s25, s24, 2
	s_add_u32 s16, s16, s25
	v_writelane_b32 v255, s28, 15
	v_readlane_b32 s48, v254, 32
	s_addc_u32 s17, s17, 0
	s_lshl_b32 s25, s86, 2
	v_writelane_b32 v255, s29, 16
	v_readlane_b32 s49, v254, 33
	s_add_u32 s28, s48, s25
	s_addc_u32 s29, s49, 0
	v_writelane_b32 v255, s28, 17
	s_and_b32 s25, s21, 0xfff00000
	s_and_b64 vcc, exec, s[0:1]
	v_writelane_b32 v255, s29, 18
	v_writelane_b32 v255, s25, 19
	s_xor_b32 s25, s23, 1
	s_lshl_b32 s25, s25, 2
	s_add_i32 s25, s25, 0
	s_add_i32 s25, s25, 0x21040
	v_writelane_b32 v255, s25, 21
	s_mov_b64 s[28:29], -1
	v_readlane_b32 s37, v254, 21
	v_readlane_b32 s38, v254, 22
	v_readlane_b32 s39, v254, 23
	v_readlane_b32 s40, v254, 24
	v_readlane_b32 s41, v254, 25
	v_readlane_b32 s42, v254, 26
	v_readlane_b32 s43, v254, 27
	v_readlane_b32 s44, v254, 28
	v_readlane_b32 s45, v254, 29
	v_readlane_b32 s50, v254, 34
	v_readlane_b32 s51, v254, 35
	s_cbranch_vccz .LBB0_488
	v_mbcnt_lo_u32_b32 v0, -1, 0
	v_mbcnt_hi_u32_b32 v0, -1, v0
	v_readlane_b32 s0, v254, 59
	v_add_u32_e32 v0, s75, v0
	s_waitcnt vmcnt(14)
	v_mov_b32 v1, 0
	s_nop 4
	global_load_dword v7, v1, s[16:17] sc1
	s_lshl_b32 s4, s4, 8
	s_waitcnt vmcnt(13)
	v_mov_b32 v1, 0
	s_nop 4
	global_load_dword v8, v1, s[16:17] sc1
	s_lshl_b32 s1, s26, 13
	v_lshrrev_b32_e32 v1, 3, v0
	v_and_or_b32 v2, v1, 7, s0
	s_add_i32 s0, s27, -1
	v_add_u32_e32 v1, s4, v2
	v_min_i32_e32 v1, s0, v1
	v_add_u32_e32 v4, s1, v1
	v_readlane_b32 s36, v254, 2
	v_ashrrev_i32_e32 v5, 31, v4
	v_readlane_b32 s48, v254, 14
	v_readlane_b32 s49, v254, 15
	v_add_u32_e32 v1, 64, v2
	v_writelane_b32 v255, s4, 23
	v_lshl_add_u64 v[4:5], v[4:5], 2, s[48:49]
	global_load_dword v3, v[4:5], off
	v_add_u32_e32 v4, s4, v1
	v_min_i32_e32 v4, s0, v4
	v_add_u32_e32 v4, s1, v4
	v_ashrrev_i32_e32 v5, 31, v4
	v_lshl_add_u64 v[4:5], v[4:5], 2, s[48:49]
	s_bitset1_b32 s4, 7
	global_load_dword v4, v[4:5], off
	v_add_u32_e32 v5, s4, v2
	v_min_i32_e32 v5, s0, v5
	v_add_u32_e32 v10, s1, v5
	v_ashrrev_i32_e32 v11, 31, v10
	v_add_u32_e32 v1, s4, v1
	v_lshl_add_u64 v[10:11], v[10:11], 2, s[48:49]
	v_min_i32_e32 v1, s0, v1
	global_load_dword v5, v[10:11], off
	v_add_u32_e32 v10, s1, v1
	v_ashrrev_i32_e32 v11, 31, v10
	v_lshl_add_u64 v[10:11], v[10:11], 2, s[48:49]
	global_load_dword v6, v[10:11], off
	s_movk_i32 s0, 0x100
	v_cmp_gt_i32_e32 vcc, s0, v0
	v_readlane_b32 s37, v254, 3
	v_readlane_b32 s38, v254, 4
	v_readlane_b32 s39, v254, 5
	v_readlane_b32 s40, v254, 6
	v_readlane_b32 s41, v254, 7
	v_readlane_b32 s42, v254, 8
	v_readlane_b32 s43, v254, 9
	v_readlane_b32 s44, v254, 10
	v_readlane_b32 s45, v254, 11
	v_readlane_b32 s46, v254, 12
	v_readlane_b32 s47, v254, 13
	v_readlane_b32 s50, v254, 16
	v_readlane_b32 s51, v254, 17
	s_and_saveexec_b64 s[0:1], vcc
	s_cbranch_execz .LBB0_460
	s_movk_i32 s4, 0x7f
	v_cmp_lt_i32_e32 vcc, s4, v0
	s_lshl_b32 s4, s26, 12
	s_lshl_b32 s25, s24, 7
	s_or_b32 s4, s4, s25
	s_and_saveexec_b64 s[28:29], vcc
	s_xor_b64 s[28:29], exec, s[28:29]
	s_cbranch_execz .LBB0_457
	v_readlane_b32 s36, v254, 40
	v_readlane_b32 s50, v254, 54
	v_readlane_b32 s51, v254, 55
	s_lshl_b32 s25, s4, 2
	s_mov_b64 s[30:31], s[50:51]
	s_add_u32 s30, s30, s25
	s_addc_u32 s31, s31, 0
	v_mov_b32_e32 v1, v150
	v_lshl_add_u64 v[10:11], v[0:1], 2, s[30:31]
	v_add_co_u32_e32 v10, vcc, 0x1000, v10
	v_readlane_b32 s37, v254, 41
	s_nop 0
	v_addc_co_u32_e32 v11, vcc, 0, v11, vcc
	global_load_dword v1, v[10:11], off offset:3584
	v_readlane_b32 s38, v254, 42
	v_readlane_b32 s39, v254, 43
	v_readlane_b32 s40, v254, 44
	v_readlane_b32 s41, v254, 45
	v_readlane_b32 s42, v254, 46
	v_readlane_b32 s43, v254, 47
	v_readlane_b32 s44, v254, 48
	v_readlane_b32 s45, v254, 49
	v_readlane_b32 s46, v254, 50
	v_readlane_b32 s47, v254, 51
	v_readlane_b32 s48, v254, 52
	v_readlane_b32 s49, v254, 53
	s_waitcnt vmcnt(0)
	v_add_f32_e32 v1, 1.0, v1

; template <int EPI>
; __device__ __forceinline__ void gemm_tile_img(const GemmArgs& g, int pm, int pn, int e, int ebase, int ecnt, LAS3 char* lds, int wid, const unsigned char* img, const TileSync& sy, int kh = -1) {
;     ...
;     if (EPI >= 2) { fl0 = ld_early(sy.flag); dp0 = ld_early(sy.dep ? sy.dep : sy.flag); }
;     unsigned aoff[2][2];
; #pragma unroll
;     for (int h = 0; h < 2; ++h)
; #pragma unroll
;         for (int i = 0; i < 2; ++i) {
;             const int rih = (i * 8 + wid) * 8 + (lane >> 3);
;             const int chunk = (lane & 7) ^ ((rih >> 1) & 7);
;             int r = pm * 256 + h * 128 + rih;
;             unsigned grow;
;             if (EPI == 2) { if (r >= ecnt) r = ecnt - 1; grow = (unsigned)(g.list[e * T + r] >> 2); }
;             else if (EPI == 3) { grow = (unsigned)(((g.abase >> 8) + pm) * (16 * 256) + h * 128 + rih); }
;             else grow = (unsigned)r;
;             aoff[h][i] = (EPI == 3) ? (grow * 128u + (unsigned)(chunk * 16)) : (EPI >= 2) ? (grow * (unsigned)D + (unsigned)(chunk * 16)) : (grow * (unsigned)D + (unsigned)(chunk * 8)) * 2u;
;         }
;     if (EPI >= 2) {
;         if (tid < 256) {
;             float bvv;
;             if (EPI == 2) bvv = (tid < 128) ? g.bias[(size_t)e * (2 * DFF) + pn * 128 + tid] : g.bias[(size_t)e * (2 * DFF) + DFF + pn * 128 + (tid - 128)] + 1.0f;
;             else bvv = g.bias[(size_t)e * D + pn * 256 + tid];
;             *(LAS3 float*)(lds + LDS_BIAS + tid * 4) = bvv;
;         }
; template <int EPI>
; __device__ __forceinline__ int* moe_phase(const Params& p, LAS3 char* lds, int wid, int* pend_in) {
;     ...
;             } else if (sl >= 0 && sl < NS) {
;                 const int e = qq + 8 * (sl / NCOL), pn = sl % NCOL;
;                 const int ecnt = __builtin_amdgcn_readfirstlane(xcnt[e]), ebase = __builtin_amdgcn_readfirstlane(xcnt[32 + e]), abase = __builtin_amdgcn_readfirstlane(xcnt[64 + e]); g.abase = abase;
;                 if (k < ((ecnt + 255) >> 8)) {
;                     TileSync sy{}; sy.flag = p.flag + ((EPI == 2) ? 0 : NE * 16) + e * NCOL + pn; sy.qctr = qctr + qq; sy.qtag = (unsigned)qq << 20; sy.qslot = slot + (par ^ 1);
;                     if (MOE_MERGED) { sy.pend = pend; if (EPI == 3) { sy.dep = p.done + e * 32 + k; sy.depn = 16; } }
;                     unsigned char* img = ((EPI == 2) ? p.img_gu : p.img_dn) + (size_t)(e * NCOL + pn) * 524288;
.LBB0_543:
	s_lshl_b32 s4, s12, 3
	v_readlane_b32 s36, v254, 20
	s_xor_b64 s[30:31], s[0:1], -1
	s_add_i32 s15, s14, s19
	s_and_b32 s15, s15, 7
	s_lshl_b64 s[0:1], s[4:5], 2
	v_readlane_b32 s46, v254, 30
	v_readlane_b32 s47, v254, 31
	s_add_u32 s0, s46, s0
	s_addc_u32 s1, s47, s1
	s_lshl_b32 s26, s15, 2
	s_add_u32 s0, s0, s26
	s_addc_u32 s1, s1, 0
	s_add_u32 s26, s0, 0x800
	s_addc_u32 s27, s1, 0
	s_lshl_b32 s0, s19, 2
	s_add_u32 s28, s2, s0
	s_addc_u32 s29, s3, 0
	s_xor_b32 s0, s10, 1
	s_lshl_b32 s0, s0, 2
	s_add_i32 s0, s0, 0
	s_and_b32 s11, s25, 0xfff00000
	s_add_i32 s35, s0, 0x21040
	s_mov_b64 s[0:1], -1
	s_and_b64 vcc, exec, s[30:31]
	v_readlane_b32 s37, v254, 21
	v_readlane_b32 s38, v254, 22
	v_readlane_b32 s39, v254, 23
	v_readlane_b32 s40, v254, 24
	v_readlane_b32 s41, v254, 25
	v_readlane_b32 s42, v254, 26
	v_readlane_b32 s43, v254, 27
	v_readlane_b32 s44, v254, 28
	v_readlane_b32 s45, v254, 29
	v_readlane_b32 s48, v254, 32
	v_readlane_b32 s49, v254, 33
	v_readlane_b32 s50, v254, 34
	v_readlane_b32 s51, v254, 35
	s_cbranch_vccz .LBB0_586
	s_lshl_b32 s0, s12, 5
	s_mov_b32 s1, s5
	v_readlane_b32 s36, v254, 20
	s_lshl_b64 s[0:1], s[0:1], 2
	v_readlane_b32 s50, v254, 34
	v_readlane_b32 s51, v254, 35
	s_add_u32 s30, s50, s0
	s_addc_u32 s31, s51, s1
	s_ashr_i32 s25, s24, 31
	s_lshl_b64 s[0:1], s[24:25], 2
	v_writelane_b32 v255, s35, 15
	s_add_u32 s0, s30, s0
	s_addc_u32 s1, s31, s1
	v_mbcnt_lo_u32_b32 v0, -1, 0
	v_mbcnt_hi_u32_b32 v0, -1, v0
	v_readlane_b32 s30, v255, 0
	v_add_u32_e32 v0, s75, v0
	v_readlane_b32 s31, v255, 1
	v_mov_b32 v1, 0
	s_nop 4
	global_load_dword v3, v1, s[26:27] sc1
	s_and_b64 s[30:31], s[30:31], exec
	s_cselect_b32 s31, s1, s27
	s_cselect_b32 s30, s0, s26
	v_mov_b32 v1, 0
	s_nop 4
	global_load_dword v2, v1, s[30:31] sc1
	s_movk_i32 s25, 0x100
	v_cmp_gt_i32_e32 vcc, s25, v0
	v_readlane_b32 s37, v254, 21
	v_readlane_b32 s38, v254, 22
	v_readlane_b32 s39, v254, 23
	v_readlane_b32 s40, v254, 24
	v_readlane_b32 s41, v254, 25
	v_readlane_b32 s42, v254, 26
	v_readlane_b32 s43, v254, 27
	v_readlane_b32 s44, v254, 28
	v_readlane_b32 s45, v254, 29
	v_readlane_b32 s46, v254, 30
	v_readlane_b32 s47, v254, 31
	v_readlane_b32 s48, v254, 32
	v_readlane_b32 s49, v254, 33
	s_and_saveexec_b64 s[30:31], vcc
	s_cbranch_execz .LBB0_546
	s_lshl_b32 s25, s12, 11
	s_lshl_b32 s34, s15, 8
	s_or_b32 s34, s25, s34
	s_mov_b32 s35, s5
	v_readlane_b32 s36, v254, 2
	s_lshl_b64 s[34:35], s[34:35], 2
	v_readlane_b32 s38, v254, 4
	v_readlane_b32 s39, v254, 5
	s_add_u32 s34, s38, s34
	s_addc_u32 s35, s39, s35
	v_ashrrev_i32_e32 v1, 31, v0
	s_waitcnt vmcnt(14)
	v_lshl_add_u64 v[4:5], v[0:1], 2, s[34:35]
	global_load_dword v4, v[4:5], off
	v_lshl_add_u32 v1, v0, 2, 0
	v_add_u32_e32 v1, 0x21c00, v1
	v_readlane_b32 s37, v254, 3
	v_readlane_b32 s40, v254, 6
	v_readlane_b32 s41, v254, 7
	v_readlane_b32 s42, v254, 8
	v_readlane_b32 s43, v254, 9
	v_readlane_b32 s44, v254, 10
	v_readlane_b32 s45, v254, 11
	v_readlane_b32 s46, v254, 12
	v_readlane_b32 s47, v254, 13
	v_readlane_b32 s48, v254, 14
	v_readlane_b32 s49, v254, 15
	v_readlane_b32 s50, v254, 16
	v_readlane_b32 s51, v254, 17
	s_waitcnt vmcnt(0)
	ds_write_b32 v1, v4
